# LSTM cell updates issued as contiguous VALU bursts between MFMA segments instead of finely interleaved
# speedup vs baseline: 1.0033x; 1.0033x over previous
.Lskipy77:
	s_waitcnt lgkmcnt(1)
	ds_read_b128 v[210:213], v243 offset:32
	v_mfma_f32_16x16x32_f16 v[174:177], v[98:101], v[214:217], v[174:177]
	v_mfma_f32_16x16x32_f16 v[178:181], v[102:105], v[214:217], v[178:181]
	v_mfma_f32_16x16x32_f16 v[182:185], v[106:109], v[214:217], v[182:185]
	v_mfma_f32_16x16x32_f16 v[186:189], v[110:113], v[214:217], v[186:189]
	global_load_dwordx4 v[234:237], v246, s[12:13]
	s_waitcnt lgkmcnt(1)
	ds_read_b128 v[214:217], v243 offset:48
	v_mfma_f32_16x16x32_f16 v[174:177], v[114:117], v[206:209], v[174:177]
	v_mfma_f32_16x16x32_f16 v[178:181], v[118:121], v[206:209], v[178:181]
	v_mfma_f32_16x16x32_f16 v[182:185], v[122:125], v[206:209], v[182:185]
	v_mfma_f32_16x16x32_f16 v[186:189], v[126:129], v[206:209], v[186:189]
	global_load_dwordx4 v[238:241], v247, s[8:9]
	s_waitcnt lgkmcnt(1)
	ds_read_b128 v[206:209], v242 offset:2304
	v_mfma_f32_16x16x32_f16 v[174:177], v[130:133], v[210:213], v[174:177]
	v_mfma_f32_16x16x32_f16 v[178:181], v[134:137], v[210:213], v[178:181]
	v_mfma_f32_16x16x32_f16 v[182:185], v[138:141], v[210:213], v[182:185]
	v_mfma_f32_16x16x32_f16 v[186:189], v[142:145], v[210:213], v[186:189]
	s_add_u32 s12, s12, 0x271000
	s_waitcnt lgkmcnt(1)
	ds_read_b128 v[210:213], v242 offset:2320
	v_mfma_f32_16x16x32_f16 v[174:177], v[146:149], v[214:217], v[174:177]
	v_mfma_f32_16x16x32_f16 v[178:181], v[150:153], v[214:217], v[178:181]
	v_mfma_f32_16x16x32_f16 v[182:185], v[154:157], v[214:217], v[182:185]
	v_mfma_f32_16x16x32_f16 v[186:189], v[158:161], v[214:217], v[186:189]
	s_addc_u32 s13, s13, 0
	s_waitcnt lgkmcnt(1)
	ds_read_b128 v[214:217], v242 offset:2400
	v_mfma_f32_16x16x32_f16 v[190:193], v[2:5], v[206:209], v[190:193]
	v_mfma_f32_16x16x32_f16 v[194:197], v[6:9], v[206:209], v[194:197]
	v_mfma_f32_16x16x32_f16 v[198:201], v[10:13], v[206:209], v[198:201]
	v_mfma_f32_16x16x32_f16 v[202:205], v[14:17], v[206:209], v[202:205]
	s_waitcnt lgkmcnt(1)
	ds_read_b128 v[206:209], v242 offset:2336
	v_mfma_f32_16x16x32_f16 v[190:193], v[18:21], v[210:213], v[190:193]
	v_mfma_f32_16x16x32_f16 v[194:197], v[22:25], v[210:213], v[194:197]
	v_mfma_f32_16x16x32_f16 v[198:201], v[26:29], v[210:213], v[198:201]
	v_mfma_f32_16x16x32_f16 v[202:205], v[30:33], v[210:213], v[202:205]
	v_exp_f32_e32 v174, v174
	v_exp_f32_e32 v175, v175
	v_exp_f32_e32 v176, v176
	v_exp_f32_e32 v177, v177
	v_exp_f32_e32 v178, v178
	v_exp_f32_e32 v179, v179
	v_exp_f32_e32 v180, v180
	v_exp_f32_e32 v181, v181
	v_exp_f32_e32 v182, v182
	v_exp_f32_e32 v183, v183
	v_exp_f32_e32 v184, v184
	v_exp_f32_e32 v185, v185
	v_exp_f32_e32 v186, v186
	v_exp_f32_e32 v187, v187
	v_exp_f32_e32 v188, v188
	v_exp_f32_e32 v189, v189
	v_add_f32_e32 v182, 1.0, v182
	v_add_f32_e32 v183, 1.0, v183
	v_add_f32_e32 v184, 1.0, v184
	v_add_f32_e32 v185, 1.0, v185
	v_add_f32_e32 v178, 1.0, v178
	v_add_f32_e32 v179, 1.0, v179
	v_add_f32_e32 v180, 1.0, v180
	v_add_f32_e32 v181, 1.0, v181
	v_fma_f32 v174, v174, v182, v182
	v_fma_f32 v175, v175, v183, v183
	v_fma_f32 v176, v176, v184, v184
	v_fma_f32 v177, v177, v185, v185
	v_rcp_f32_e32 v178, v178
	v_rcp_f32_e32 v179, v179
	v_rcp_f32_e32 v180, v180
	v_rcp_f32_e32 v181, v181
	v_fma_f32 v182, v182, v252, s16
	v_fma_f32 v183, v183, v252, s16
	v_fma_f32 v184, v184, v252, s16
	v_fma_f32 v185, v185, v252, s16
	v_rcp_f32_e32 v174, v174
	v_rcp_f32_e32 v175, v175
	v_rcp_f32_e32 v176, v176
	v_rcp_f32_e32 v177, v177
	v_mul_f32_e32 v162, v162, v178
	v_mul_f32_e32 v163, v163, v179
	v_mul_f32_e32 v164, v164, v180
	v_mul_f32_e32 v165, v165, v181
	v_fma_f32 v162, v182, v174, v162
	v_fma_f32 v163, v183, v175, v163
	v_fma_f32 v164, v184, v176, v164
	v_fma_f32 v165, v185, v177, v165
	v_exp_f32_e32 v178, v162
	v_exp_f32_e32 v179, v163
	v_exp_f32_e32 v180, v164
	v_exp_f32_e32 v181, v165
	v_add_f32_e32 v174, 1.0, v178
	v_add_f32_e32 v175, 1.0, v179
	v_add_f32_e32 v176, 1.0, v180
	v_add_f32_e32 v177, 1.0, v181
	v_add_f32_e32 v182, -1.0, v178
	v_add_f32_e32 v183, -1.0, v179
	v_add_f32_e32 v184, -1.0, v180
	v_add_f32_e32 v185, -1.0, v181
	v_fma_f32 v186, v186, v174, v174
	v_fma_f32 v187, v187, v175, v175
	v_fma_f32 v188, v188, v176, v176
	v_fma_f32 v189, v189, v177, v177
	v_rcp_f32_e32 v186, v186
	v_rcp_f32_e32 v187, v187
	v_rcp_f32_e32 v188, v188
	v_rcp_f32_e32 v189, v189
	v_mul_f32_e32 v186, v182, v186
	v_mul_f32_e32 v187, v183, v187
	v_mul_f32_e32 v188, v184, v188
	v_mul_f32_e32 v189, v185, v189
	v_cvt_pk_f16_f32 v186, v186, v187
	v_cvt_pk_f16_f32 v187, v188, v189
	ds_write_b64 v244, v[186:187] offset:15360
	ds_read_b128 v[174:177], v245 offset:0
	ds_read_b128 v[178:181], v245 offset:512
	ds_read_b128 v[182:185], v245 offset:1024
	ds_read_b128 v[186:189], v245 offset:1536
	s_waitcnt lgkmcnt(6)
	ds_read_b128 v[210:213], v242 offset:2352
	v_mfma_f32_16x16x32_f16 v[190:193], v[218:221], v[214:217], v[190:193]
	ds_read_b128 v[218:221], v255 offset:4096
	v_mfma_f32_16x16x32_f16 v[194:197], v[222:225], v[214:217], v[194:197]
	ds_read_b128 v[222:225], v255 offset:5120
	v_mfma_f32_16x16x32_f16 v[198:201], v[226:229], v[214:217], v[198:201]
	ds_read_b128 v[226:229], v255 offset:6144
	v_mfma_f32_16x16x32_f16 v[202:205], v[230:233], v[214:217], v[202:205]
	ds_read_b128 v[230:233], v255 offset:7168
	s_waitcnt lgkmcnt(10)
	ds_read_b128 v[214:217], v243 offset:1280
	v_mfma_f32_16x16x32_f16 v[190:193], v[34:37], v[206:209], v[190:193]
	v_mfma_f32_16x16x32_f16 v[194:197], v[38:41], v[206:209], v[194:197]
	v_mfma_f32_16x16x32_f16 v[198:201], v[42:45], v[206:209], v[198:201]
	v_mfma_f32_16x16x32_f16 v[202:205], v[46:49], v[206:209], v[202:205]
	s_waitcnt lgkmcnt(5)
	ds_read_b128 v[206:209], v243 offset:1296
	v_mfma_f32_16x16x32_f16 v[190:193], v[50:53], v[210:213], v[190:193]
	v_mfma_f32_16x16x32_f16 v[194:197], v[54:57], v[210:213], v[194:197]
	v_mfma_f32_16x16x32_f16 v[198:201], v[58:61], v[210:213], v[198:201]
	v_mfma_f32_16x16x32_f16 v[202:205], v[62:65], v[210:213], v[202:205]
	s_waitcnt lgkmcnt(1)
	ds_read_b128 v[210:213], v242 offset:2416
	v_mfma_f32_16x16x32_f16 v[190:193], v[98:101], v[214:217], v[190:193]
	v_mfma_f32_16x16x32_f16 v[194:197], v[102:105], v[214:217], v[194:197]
	v_mfma_f32_16x16x32_f16 v[198:201], v[106:109], v[214:217], v[198:201]
	v_mfma_f32_16x16x32_f16 v[202:205], v[110:113], v[214:217], v[202:205]
	s_waitcnt lgkmcnt(1)
	ds_read_b128 v[214:217], v242 offset:2368
	v_mfma_f32_16x16x32_f16 v[190:193], v[114:117], v[206:209], v[190:193]
	v_mfma_f32_16x16x32_f16 v[194:197], v[118:121], v[206:209], v[194:197]
	v_mfma_f32_16x16x32_f16 v[198:201], v[122:125], v[206:209], v[198:201]
	v_mfma_f32_16x16x32_f16 v[202:205], v[126:129], v[206:209], v[202:205]
	s_waitcnt lgkmcnt(1)
	ds_read_b128 v[206:209], v242 offset:2384
	v_mfma_f32_16x16x32_f16 v[190:193], v[218:221], v[210:213], v[190:193]
	ds_read_b128 v[218:221], v255 offset:0
	v_mfma_f32_16x16x32_f16 v[194:197], v[222:225], v[210:213], v[194:197]
	ds_read_b128 v[222:225], v255 offset:1024
	v_mfma_f32_16x16x32_f16 v[198:201], v[226:229], v[210:213], v[198:201]
	ds_read_b128 v[226:229], v255 offset:2048
	v_mfma_f32_16x16x32_f16 v[202:205], v[230:233], v[210:213], v[202:205]
	ds_read_b128 v[230:233], v255 offset:3072
	s_waitcnt lgkmcnt(5)
	ds_read_b128 v[210:213], v243 offset:1312
	v_mfma_f32_16x16x32_f16 v[190:193], v[66:69], v[214:217], v[190:193]
	v_mfma_f32_16x16x32_f16 v[194:197], v[70:73], v[214:217], v[194:197]
	v_mfma_f32_16x16x32_f16 v[198:201], v[74:77], v[214:217], v[198:201]
	v_mfma_f32_16x16x32_f16 v[202:205], v[78:81], v[214:217], v[202:205]
	s_waitcnt lgkmcnt(5)
	ds_read_b128 v[214:217], v243 offset:1328
	v_mfma_f32_16x16x32_f16 v[190:193], v[82:85], v[206:209], v[190:193]
	v_mfma_f32_16x16x32_f16 v[194:197], v[86:89], v[206:209], v[194:197]
	v_mfma_f32_16x16x32_f16 v[198:201], v[90:93], v[206:209], v[198:201]
	v_mfma_f32_16x16x32_f16 v[202:205], v[94:97], v[206:209], v[202:205]
	s_waitcnt vmcnt(0)
	ds_write_b128 v249, v[234:237] offset:0
	ds_write_b128 v249, v[238:241] offset:29952
	global_load_dwordx4 v[234:237], v248, s[8:9]
	s_add_u32 s8, s8, 0x271000
	s_addc_u32 s9, s9, 0
	s_waitcnt lgkmcnt(3)
	ds_read_b128 v[206:209], v242 offset:4608
	v_mfma_f32_16x16x32_f16 v[190:193], v[130:133], v[210:213], v[190:193]
	v_mfma_f32_16x16x32_f16 v[194:197], v[134:137], v[210:213], v[194:197]
	v_mfma_f32_16x16x32_f16 v[198:201], v[138:141], v[210:213], v[198:201]
	v_mfma_f32_16x16x32_f16 v[202:205], v[142:145], v[210:213], v[202:205]
	s_waitcnt lgkmcnt(3)
	ds_read_b128 v[210:213], v242 offset:4624
	v_mfma_f32_16x16x32_f16 v[190:193], v[146:149], v[214:217], v[190:193]
	v_mfma_f32_16x16x32_f16 v[194:197], v[150:153], v[214:217], v[194:197]
	v_mfma_f32_16x16x32_f16 v[198:201], v[154:157], v[214:217], v[198:201]
	v_mfma_f32_16x16x32_f16 v[202:205], v[158:161], v[214:217], v[202:205]
	s_waitcnt lgkmcnt(1)
	ds_read_b128 v[214:217], v242 offset:4704
	v_mfma_f32_16x16x32_f16 v[174:177], v[2:5], v[206:209], v[174:177]
	v_mfma_f32_16x16x32_f16 v[178:181], v[6:9], v[206:209], v[178:181]
	v_mfma_f32_16x16x32_f16 v[182:185], v[10:13], v[206:209], v[182:185]
	v_mfma_f32_16x16x32_f16 v[186:189], v[14:17], v[206:209], v[186:189]
	s_waitcnt lgkmcnt(1)
	ds_read_b128 v[206:209], v242 offset:4640
	v_mfma_f32_16x16x32_f16 v[174:177], v[18:21], v[210:213], v[174:177]
	v_mfma_f32_16x16x32_f16 v[178:181], v[22:25], v[210:213], v[178:181]
	v_mfma_f32_16x16x32_f16 v[182:185], v[26:29], v[210:213], v[182:185]
	v_mfma_f32_16x16x32_f16 v[186:189], v[30:33], v[210:213], v[186:189]
	v_exp_f32_e32 v190, v190
	v_exp_f32_e32 v191, v191
	v_exp_f32_e32 v192, v192
	v_exp_f32_e32 v193, v193
	v_exp_f32_e32 v194, v194
	v_exp_f32_e32 v195, v195
	v_exp_f32_e32 v196, v196
	v_exp_f32_e32 v197, v197
	v_exp_f32_e32 v198, v198
	v_exp_f32_e32 v199, v199
	v_exp_f32_e32 v200, v200
	v_exp_f32_e32 v201, v201
	v_exp_f32_e32 v202, v202
	v_exp_f32_e32 v203, v203
	v_exp_f32_e32 v204, v204
	v_exp_f32_e32 v205, v205
	v_add_f32_e32 v198, 1.0, v198
	v_add_f32_e32 v199, 1.0, v199
	v_add_f32_e32 v200, 1.0, v200
	v_add_f32_e32 v201, 1.0, v201
	v_add_f32_e32 v194, 1.0, v194
	v_add_f32_e32 v195, 1.0, v195
	v_add_f32_e32 v196, 1.0, v196
	v_add_f32_e32 v197, 1.0, v197
	v_fma_f32 v190, v190, v198, v198
	v_fma_f32 v191, v191, v199, v199
	v_fma_f32 v192, v192, v200, v200
	v_fma_f32 v193, v193, v201, v201
	v_rcp_f32_e32 v194, v194
	v_rcp_f32_e32 v195, v195
	v_rcp_f32_e32 v196, v196
	v_rcp_f32_e32 v197, v197
	v_fma_f32 v198, v198, v252, s16
	v_fma_f32 v199, v199, v252, s16
	v_fma_f32 v200, v200, v252, s16
	v_fma_f32 v201, v201, v252, s16
	v_rcp_f32_e32 v190, v190
	v_rcp_f32_e32 v191, v191
	v_rcp_f32_e32 v192, v192
	v_rcp_f32_e32 v193, v193
	v_mul_f32_e32 v166, v166, v194
	v_mul_f32_e32 v167, v167, v195
	v_mul_f32_e32 v168, v168, v196
	v_mul_f32_e32 v169, v169, v197
	v_fma_f32 v166, v198, v190, v166
	v_fma_f32 v167, v199, v191, v167
	v_fma_f32 v168, v200, v192, v168
	v_fma_f32 v169, v201, v193, v169
	v_exp_f32_e32 v194, v166
	v_exp_f32_e32 v195, v167
	v_exp_f32_e32 v196, v168
	v_exp_f32_e32 v197, v169
	v_add_f32_e32 v190, 1.0, v194
	v_add_f32_e32 v191, 1.0, v195
	v_add_f32_e32 v192, 1.0, v196
	v_add_f32_e32 v193, 1.0, v197
	v_add_f32_e32 v198, -1.0, v194
	v_add_f32_e32 v199, -1.0, v195
	v_add_f32_e32 v200, -1.0, v196
	v_add_f32_e32 v201, -1.0, v197
	v_fma_f32 v202, v202, v190, v190
	v_fma_f32 v203, v203, v191, v191
	v_fma_f32 v204, v204, v192, v192
	v_fma_f32 v205, v205, v193, v193
	v_rcp_f32_e32 v202, v202
	v_rcp_f32_e32 v203, v203
	v_rcp_f32_e32 v204, v204
	v_rcp_f32_e32 v205, v205
	v_mul_f32_e32 v202, v198, v202
	v_mul_f32_e32 v203, v199, v203
	v_mul_f32_e32 v204, v200, v204
	v_mul_f32_e32 v205, v201, v205
	v_cvt_pk_f16_f32 v202, v202, v203
	v_cvt_pk_f16_f32 v203, v204, v205
	ds_write_b64 v244, v[202:203] offset:16640
	ds_read_b128 v[190:193], v245 offset:0
	ds_read_b128 v[194:197], v245 offset:512
	ds_read_b128 v[198:201], v245 offset:1024
	ds_read_b128 v[202:205], v245 offset:1536
	s_waitcnt lgkmcnt(6)
	ds_read_b128 v[210:213], v242 offset:4656
	v_mfma_f32_16x16x32_f16 v[174:177], v[218:221], v[214:217], v[174:177]
	ds_read_b128 v[218:221], v255 offset:4096
	v_mfma_f32_16x16x32_f16 v[178:181], v[222:225], v[214:217], v[178:181]
	ds_read_b128 v[222:225], v255 offset:5120
	v_mfma_f32_16x16x32_f16 v[182:185], v[226:229], v[214:217], v[182:185]
	ds_read_b128 v[226:229], v255 offset:6144
	v_mfma_f32_16x16x32_f16 v[186:189], v[230:233], v[214:217], v[186:189]
	ds_read_b128 v[230:233], v255 offset:7168
	s_waitcnt lgkmcnt(10)
	ds_read_b128 v[214:217], v243 offset:2560
	v_mfma_f32_16x16x32_f16 v[174:177], v[34:37], v[206:209], v[174:177]
	v_mfma_f32_16x16x32_f16 v[178:181], v[38:41], v[206:209], v[178:181]
	v_mfma_f32_16x16x32_f16 v[182:185], v[42:45], v[206:209], v[182:185]
	v_mfma_f32_16x16x32_f16 v[186:189], v[46:49], v[206:209], v[186:189]
	s_waitcnt lgkmcnt(5)
	ds_read_b128 v[206:209], v243 offset:2576
	v_mfma_f32_16x16x32_f16 v[174:177], v[50:53], v[210:213], v[174:177]
	v_mfma_f32_16x16x32_f16 v[178:181], v[54:57], v[210:213], v[178:181]
	v_mfma_f32_16x16x32_f16 v[182:185], v[58:61], v[210:213], v[182:185]
	v_mfma_f32_16x16x32_f16 v[186:189], v[62:65], v[210:213], v[186:189]
	s_waitcnt lgkmcnt(1)
	ds_read_b128 v[210:213], v242 offset:4720
	v_mfma_f32_16x16x32_f16 v[174:177], v[98:101], v[214:217], v[174:177]
	v_mfma_f32_16x16x32_f16 v[178:181], v[102:105], v[214:217], v[178:181]
	v_mfma_f32_16x16x32_f16 v[182:185], v[106:109], v[214:217], v[182:185]
	v_mfma_f32_16x16x32_f16 v[186:189], v[110:113], v[214:217], v[186:189]
	s_waitcnt lgkmcnt(1)
	ds_read_b128 v[214:217], v242 offset:4672
	v_mfma_f32_16x16x32_f16 v[174:177], v[114:117], v[206:209], v[174:177]
	v_mfma_f32_16x16x32_f16 v[178:181], v[118:121], v[206:209], v[178:181]
	v_mfma_f32_16x16x32_f16 v[182:185], v[122:125], v[206:209], v[182:185]
	v_mfma_f32_16x16x32_f16 v[186:189], v[126:129], v[206:209], v[186:189]
	s_waitcnt lgkmcnt(1)
	ds_read_b128 v[206:209], v242 offset:4688
	v_mfma_f32_16x16x32_f16 v[174:177], v[218:221], v[210:213], v[174:177]
	ds_read_b128 v[218:221], v255 offset:0
	v_mfma_f32_16x16x32_f16 v[178:181], v[222:225], v[210:213], v[178:181]
	ds_read_b128 v[222:225], v255 offset:1024
	v_mfma_f32_16x16x32_f16 v[182:185], v[226:229], v[210:213], v[182:185]
	ds_read_b128 v[226:229], v255 offset:2048
	v_mfma_f32_16x16x32_f16 v[186:189], v[230:233], v[210:213], v[186:189]
	ds_read_b128 v[230:233], v255 offset:3072
	s_waitcnt lgkmcnt(5)
	ds_read_b128 v[210:213], v243 offset:2592
	v_mfma_f32_16x16x32_f16 v[174:177], v[66:69], v[214:217], v[174:177]
	v_mfma_f32_16x16x32_f16 v[178:181], v[70:73], v[214:217], v[178:181]
	v_mfma_f32_16x16x32_f16 v[182:185], v[74:77], v[214:217], v[182:185]
	v_mfma_f32_16x16x32_f16 v[186:189], v[78:81], v[214:217], v[186:189]
	s_waitcnt lgkmcnt(5)
	ds_read_b128 v[214:217], v243 offset:2608
	v_mfma_f32_16x16x32_f16 v[174:177], v[82:85], v[206:209], v[174:177]
	v_mfma_f32_16x16x32_f16 v[178:181], v[86:89], v[206:209], v[178:181]
	v_mfma_f32_16x16x32_f16 v[182:185], v[90:93], v[206:209], v[182:185]
	v_mfma_f32_16x16x32_f16 v[186:189], v[94:97], v[206:209], v[186:189]
	s_waitcnt lgkmcnt(1)
	ds_read_b128 v[206:209], v242 offset:27648
	v_mfma_f32_16x16x32_f16 v[174:177], v[130:133], v[210:213], v[174:177]
	v_mfma_f32_16x16x32_f16 v[178:181], v[134:137], v[210:213], v[178:181]
	v_mfma_f32_16x16x32_f16 v[182:185], v[138:141], v[210:213], v[182:185]
	v_mfma_f32_16x16x32_f16 v[186:189], v[142:145], v[210:213], v[186:189]
	s_waitcnt lgkmcnt(1)
	ds_read_b128 v[210:213], v242 offset:27744
	v_mfma_f32_16x16x32_f16 v[174:177], v[146:149], v[214:217], v[174:177]
	v_mfma_f32_16x16x32_f16 v[178:181], v[150:153], v[214:217], v[178:181]
	v_mfma_f32_16x16x32_f16 v[182:185], v[154:157], v[214:217], v[182:185]
	v_mfma_f32_16x16x32_f16 v[186:189], v[158:161], v[214:217], v[186:189]
	s_waitcnt vmcnt(0)
	ds_write_b128 v249, v[234:237] offset:32256
	s_waitcnt lgkmcnt(2)
	ds_read_b128 v[214:217], v242 offset:27664
	v_mfma_f32_16x16x32_f16 v[190:193], v[2:5], v[206:209], v[190:193]
	v_mfma_f32_16x16x32_f16 v[194:197], v[6:9], v[206:209], v[194:197]
	v_mfma_f32_16x16x32_f16 v[198:201], v[10:13], v[206:209], v[198:201]
	v_mfma_f32_16x16x32_f16 v[202:205], v[14:17], v[206:209], v[202:205]
	s_waitcnt lgkmcnt(2)
	ds_read_b128 v[206:209], v242 offset:27680
	v_mfma_f32_16x16x32_f16 v[190:193], v[218:221], v[210:213], v[190:193]
	ds_read_b128 v[218:221], v255 offset:4096
	v_mfma_f32_16x16x32_f16 v[194:197], v[222:225], v[210:213], v[194:197]
	ds_read_b128 v[222:225], v255 offset:5120
	v_mfma_f32_16x16x32_f16 v[198:201], v[226:229], v[210:213], v[198:201]
	ds_read_b128 v[226:229], v255 offset:6144
	v_mfma_f32_16x16x32_f16 v[202:205], v[230:233], v[210:213], v[202:205]
	ds_read_b128 v[230:233], v255 offset:7168
	v_exp_f32_e32 v174, v174
	v_exp_f32_e32 v175, v175
	v_exp_f32_e32 v176, v176
	v_exp_f32_e32 v177, v177
	v_exp_f32_e32 v178, v178
	v_exp_f32_e32 v179, v179
	v_exp_f32_e32 v180, v180
	v_exp_f32_e32 v181, v181
	v_exp_f32_e32 v182, v182
	v_exp_f32_e32 v183, v183
	v_exp_f32_e32 v184, v184
	v_exp_f32_e32 v185, v185
	v_exp_f32_e32 v186, v186
	v_exp_f32_e32 v187, v187
	v_exp_f32_e32 v188, v188
	v_exp_f32_e32 v189, v189
	v_add_f32_e32 v182, 1.0, v182
	v_add_f32_e32 v183, 1.0, v183
	v_add_f32_e32 v184, 1.0, v184
	v_add_f32_e32 v185, 1.0, v185
	v_add_f32_e32 v178, 1.0, v178
	v_add_f32_e32 v179, 1.0, v179
	v_add_f32_e32 v180, 1.0, v180
	v_add_f32_e32 v181, 1.0, v181
	v_fma_f32 v174, v174, v182, v182
	v_fma_f32 v175, v175, v183, v183
	v_fma_f32 v176, v176, v184, v184
	v_fma_f32 v177, v177, v185, v185
	v_rcp_f32_e32 v178, v178
	v_rcp_f32_e32 v179, v179
	v_rcp_f32_e32 v180, v180
	v_rcp_f32_e32 v181, v181
	v_fma_f32 v182, v182, v252, s16
	v_fma_f32 v183, v183, v252, s16
	v_fma_f32 v184, v184, v252, s16
	v_fma_f32 v185, v185, v252, s16
	v_rcp_f32_e32 v174, v174
	v_rcp_f32_e32 v175, v175
	v_rcp_f32_e32 v176, v176
	v_rcp_f32_e32 v177, v177
	v_mul_f32_e32 v170, v170, v178
	v_mul_f32_e32 v171, v171, v179
	v_mul_f32_e32 v172, v172, v180
	v_mul_f32_e32 v173, v173, v181
	v_fma_f32 v170, v182, v174, v170
	v_fma_f32 v171, v183, v175, v171
	v_fma_f32 v172, v184, v176, v172
	v_fma_f32 v173, v185, v177, v173
	v_exp_f32_e32 v178, v170
	v_exp_f32_e32 v179, v171
	v_exp_f32_e32 v180, v172
	v_exp_f32_e32 v181, v173
	v_add_f32_e32 v174, 1.0, v178
	v_add_f32_e32 v175, 1.0, v179
	v_add_f32_e32 v176, 1.0, v180
	v_add_f32_e32 v177, 1.0, v181
	v_add_f32_e32 v182, -1.0, v178
	v_add_f32_e32 v183, -1.0, v179
	v_add_f32_e32 v184, -1.0, v180
	v_add_f32_e32 v185, -1.0, v181
	v_fma_f32 v186, v186, v174, v174
	v_fma_f32 v187, v187, v175, v175
	v_fma_f32 v188, v188, v176, v176
	v_fma_f32 v189, v189, v177, v177
	v_rcp_f32_e32 v186, v186
	v_rcp_f32_e32 v187, v187
	v_rcp_f32_e32 v188, v188
	v_rcp_f32_e32 v189, v189
	v_mul_f32_e32 v186, v182, v186
	v_mul_f32_e32 v187, v183, v187
	v_mul_f32_e32 v188, v184, v188
	v_mul_f32_e32 v189, v185, v189
	v_cvt_pk_f16_f32 v186, v186, v187
	v_cvt_pk_f16_f32 v187, v188, v189
	ds_write_b64 v244, v[186:187] offset:17920
	ds_read_b128 v[174:177], v245 offset:0
	ds_read_b128 v[178:181], v245 offset:512
	ds_read_b128 v[182:185], v245 offset:1024
	ds_read_b128 v[186:189], v245 offset:1536
	s_waitcnt lgkmcnt(10)
	ds_read_b128 v[210:213], v242 offset:27760
	v_mfma_f32_16x16x32_f16 v[190:193], v[18:21], v[214:217], v[190:193]
	v_mfma_f32_16x16x32_f16 v[194:197], v[22:25], v[214:217], v[194:197]
	v_mfma_f32_16x16x32_f16 v[198:201], v[26:29], v[214:217], v[198:201]
	v_mfma_f32_16x16x32_f16 v[202:205], v[30:33], v[214:217], v[202:205]
	s_waitcnt lgkmcnt(10)
	ds_read_b128 v[214:217], v242 offset:27696
	v_mfma_f32_16x16x32_f16 v[190:193], v[34:37], v[206:209], v[190:193]
	v_mfma_f32_16x16x32_f16 v[194:197], v[38:41], v[206:209], v[194:197]
	v_mfma_f32_16x16x32_f16 v[198:201], v[42:45], v[206:209], v[198:201]
	v_mfma_f32_16x16x32_f16 v[202:205], v[46:49], v[206:209], v[202:205]
	s_waitcnt lgkmcnt(1)
	ds_read_b128 v[206:209], v242 offset:27712
	v_mfma_f32_16x16x32_f16 v[190:193], v[218:221], v[210:213], v[190:193]
	ds_read_b128 v[218:221], v255 offset:0
	v_mfma_f32_16x16x32_f16 v[194:197], v[222:225], v[210:213], v[194:197]
	ds_read_b128 v[222:225], v255 offset:1024
	v_mfma_f32_16x16x32_f16 v[198:201], v[226:229], v[210:213], v[198:201]
	ds_read_b128 v[226:229], v255 offset:2048
	v_mfma_f32_16x16x32_f16 v[202:205], v[230:233], v[210:213], v[202:205]
	ds_read_b128 v[230:233], v255 offset:3072
	s_waitcnt lgkmcnt(5)
	ds_read_b128 v[210:213], v242 offset:27728
	v_mfma_f32_16x16x32_f16 v[190:193], v[50:53], v[214:217], v[190:193]
	v_mfma_f32_16x16x32_f16 v[194:197], v[54:57], v[214:217], v[194:197]
	v_mfma_f32_16x16x32_f16 v[198:201], v[58:61], v[214:217], v[198:201]
	v_mfma_f32_16x16x32_f16 v[202:205], v[62:65], v[214:217], v[202:205]
	s_waitcnt lgkmcnt(0)
	s_barrier
	ds_read_b128 v[234:237], v250 offset:15360
	s_mov_b64 exec, s[20:21]
	ds_read_b128 v[238:241], v250 offset:17920
	s_mov_b64 exec, -1
	ds_read_b128 v[214:217], v243 offset:15360
	v_mfma_f32_16x16x32_f16 v[190:193], v[66:69], v[206:209], v[190:193]
	v_mfma_f32_16x16x32_f16 v[194:197], v[70:73], v[206:209], v[194:197]
	v_mfma_f32_16x16x32_f16 v[198:201], v[74:77], v[206:209], v[198:201]
	v_mfma_f32_16x16x32_f16 v[202:205], v[78:81], v[206:209], v[202:205]
	ds_read_b128 v[206:209], v243 offset:15376
	v_mfma_f32_16x16x32_f16 v[190:193], v[82:85], v[210:213], v[190:193]
	v_mfma_f32_16x16x32_f16 v[194:197], v[86:89], v[210:213], v[194:197]
	v_mfma_f32_16x16x32_f16 v[198:201], v[90:93], v[210:213], v[198:201]
	v_mfma_f32_16x16x32_f16 v[202:205], v[94:97], v[210:213], v[202:205]
	s_waitcnt lgkmcnt(2)
	s_mov_b64 exec, s[18:19]
	global_store_dwordx4 v251, v[234:237], s[10:11]
	s_mov_b64 exec, s[20:21]
	global_store_dwordx4 v251, v[238:241], s[14:15]
	s_mov_b64 exec, -1
	s_add_u32 s10, s10, 0x271000
	s_addc_u32 s11, s11, 0
	s_add_u32 s14, s14, 0x271000
	s_addc_u32 s15, s15, 0
	s_waitcnt lgkmcnt(1)
	ds_read_b128 v[210:213], v243 offset:15392
	v_mfma_f32_16x16x32_f16 v[190:193], v[98:101], v[214:217], v[190:193]
	v_mfma_f32_16x16x32_f16 v[194:197], v[102:105], v[214:217], v[194:197]
	v_mfma_f32_16x16x32_f16 v[198:201], v[106:109], v[214:217], v[198:201]
	v_mfma_f32_16x16x32_f16 v[202:205], v[110:113], v[214:217], v[202:205]
	global_load_dwordx4 v[234:237], v246, s[12:13]
	s_waitcnt lgkmcnt(1)
	ds_read_b128 v[214:217], v243 offset:15408
	v_mfma_f32_16x16x32_f16 v[190:193], v[114:117], v[206:209], v[190:193]
	v_mfma_f32_16x16x32_f16 v[194:197], v[118:121], v[206:209], v[194:197]
	v_mfma_f32_16x16x32_f16 v[198:201], v[122:125], v[206:209], v[198:201]
	v_mfma_f32_16x16x32_f16 v[202:205], v[126:129], v[206:209], v[202:205]
	global_load_dwordx4 v[238:241], v247, s[8:9]
	s_waitcnt lgkmcnt(1)
	ds_read_b128 v[206:209], v242 offset:29952
	v_mfma_f32_16x16x32_f16 v[190:193], v[130:133], v[210:213], v[190:193]
	v_mfma_f32_16x16x32_f16 v[194:197], v[134:137], v[210:213], v[194:197]
	v_mfma_f32_16x16x32_f16 v[198:201], v[138:141], v[210:213], v[198:201]
	v_mfma_f32_16x16x32_f16 v[202:205], v[142:145], v[210:213], v[202:205]
	s_add_u32 s12, s12, 0x271000
	s_waitcnt lgkmcnt(1)
	ds_read_b128 v[210:213], v242 offset:29968
	v_mfma_f32_16x16x32_f16 v[190:193], v[146:149], v[214:217], v[190:193]
	v_mfma_f32_16x16x32_f16 v[194:197], v[150:153], v[214:217], v[194:197]
	v_mfma_f32_16x16x32_f16 v[198:201], v[154:157], v[214:217], v[198:201]
	v_mfma_f32_16x16x32_f16 v[202:205], v[158:161], v[214:217], v[202:205]
	s_addc_u32 s13, s13, 0
	s_waitcnt lgkmcnt(1)
	ds_read_b128 v[214:217], v242 offset:30048
	v_mfma_f32_16x16x32_f16 v[174:177], v[2:5], v[206:209], v[174:177]
	v_mfma_f32_16x16x32_f16 v[178:181], v[6:9], v[206:209], v[178:181]
	v_mfma_f32_16x16x32_f16 v[182:185], v[10:13], v[206:209], v[182:185]
	v_mfma_f32_16x16x32_f16 v[186:189], v[14:17], v[206:209], v[186:189]
	s_waitcnt lgkmcnt(1)
	ds_read_b128 v[206:209], v242 offset:29984
	v_mfma_f32_16x16x32_f16 v[174:177], v[18:21], v[210:213], v[174:177]
	v_mfma_f32_16x16x32_f16 v[178:181], v[22:25], v[210:213], v[178:181]
	v_mfma_f32_16x16x32_f16 v[182:185], v[26:29], v[210:213], v[182:185]
	v_mfma_f32_16x16x32_f16 v[186:189], v[30:33], v[210:213], v[186:189]
	v_exp_f32_e32 v190, v190
	v_exp_f32_e32 v191, v191
	v_exp_f32_e32 v192, v192
	v_exp_f32_e32 v193, v193
	v_exp_f32_e32 v194, v194
	v_exp_f32_e32 v195, v195
	v_exp_f32_e32 v196, v196
	v_exp_f32_e32 v197, v197
	v_exp_f32_e32 v198, v198
	v_exp_f32_e32 v199, v199
	v_exp_f32_e32 v200, v200
	v_exp_f32_e32 v201, v201
	v_exp_f32_e32 v202, v202
	v_exp_f32_e32 v203, v203
	v_exp_f32_e32 v204, v204
	v_exp_f32_e32 v205, v205
	v_add_f32_e32 v198, 1.0, v198
	v_add_f32_e32 v199, 1.0, v199
	v_add_f32_e32 v200, 1.0, v200
	v_add_f32_e32 v201, 1.0, v201
	v_add_f32_e32 v194, 1.0, v194
	v_add_f32_e32 v195, 1.0, v195
	v_add_f32_e32 v196, 1.0, v196
	v_add_f32_e32 v197, 1.0, v197
	v_fma_f32 v190, v190, v198, v198
	v_fma_f32 v191, v191, v199, v199
	v_fma_f32 v192, v192, v200, v200
	v_fma_f32 v193, v193, v201, v201
	v_rcp_f32_e32 v194, v194
	v_rcp_f32_e32 v195, v195
	v_rcp_f32_e32 v196, v196
	v_rcp_f32_e32 v197, v197
	v_fma_f32 v198, v198, v252, s16
	v_fma_f32 v199, v199, v252, s16
	v_fma_f32 v200, v200, v252, s16
	v_fma_f32 v201, v201, v252, s16
	v_rcp_f32_e32 v190, v190
	v_rcp_f32_e32 v191, v191
	v_rcp_f32_e32 v192, v192
	v_rcp_f32_e32 v193, v193
	v_mul_f32_e32 v162, v162, v194
	v_mul_f32_e32 v163, v163, v195
	v_mul_f32_e32 v164, v164, v196
	v_mul_f32_e32 v165, v165, v197
	v_fma_f32 v162, v198, v190, v162
	v_fma_f32 v163, v199, v191, v163
	v_fma_f32 v164, v200, v192, v164
	v_fma_f32 v165, v201, v193, v165
	v_exp_f32_e32 v194, v162
	v_exp_f32_e32 v195, v163
	v_exp_f32_e32 v196, v164
	v_exp_f32_e32 v197, v165
	v_add_f32_e32 v190, 1.0, v194
	v_add_f32_e32 v191, 1.0, v195
	v_add_f32_e32 v192, 1.0, v196
	v_add_f32_e32 v193, 1.0, v197
	v_add_f32_e32 v198, -1.0, v194
	v_add_f32_e32 v199, -1.0, v195
	v_add_f32_e32 v200, -1.0, v196
	v_add_f32_e32 v201, -1.0, v197
	v_fma_f32 v202, v202, v190, v190
	v_fma_f32 v203, v203, v191, v191
	v_fma_f32 v204, v204, v192, v192
	v_fma_f32 v205, v205, v193, v193
	v_rcp_f32_e32 v202, v202
	v_rcp_f32_e32 v203, v203
	v_rcp_f32_e32 v204, v204
	v_rcp_f32_e32 v205, v205
	v_mul_f32_e32 v202, v198, v202
	v_mul_f32_e32 v203, v199, v203
	v_mul_f32_e32 v204, v200, v204
	v_mul_f32_e32 v205, v201, v205
	v_cvt_pk_f16_f32 v202, v202, v203
	v_cvt_pk_f16_f32 v203, v204, v205
	ds_write_b64 v244, v[202:203] offset:0
	ds_read_b128 v[190:193], v245 offset:0
	ds_read_b128 v[194:197], v245 offset:512
	ds_read_b128 v[198:201], v245 offset:1024
	ds_read_b128 v[202:205], v245 offset:1536
	s_waitcnt lgkmcnt(6)
	ds_read_b128 v[210:213], v242 offset:30000
	v_mfma_f32_16x16x32_f16 v[174:177], v[218:221], v[214:217], v[174:177]
	ds_read_b128 v[218:221], v255 offset:4096
	v_mfma_f32_16x16x32_f16 v[178:181], v[222:225], v[214:217], v[178:181]
	ds_read_b128 v[222:225], v255 offset:5120
	v_mfma_f32_16x16x32_f16 v[182:185], v[226:229], v[214:217], v[182:185]
	ds_read_b128 v[226:229], v255 offset:6144
	v_mfma_f32_16x16x32_f16 v[186:189], v[230:233], v[214:217], v[186:189]
	ds_read_b128 v[230:233], v255 offset:7168
	s_waitcnt lgkmcnt(10)
	ds_read_b128 v[214:217], v243 offset:16640
	v_mfma_f32_16x16x32_f16 v[174:177], v[34:37], v[206:209], v[174:177]
	v_mfma_f32_16x16x32_f16 v[178:181], v[38:41], v[206:209], v[178:181]
	v_mfma_f32_16x16x32_f16 v[182:185], v[42:45], v[206:209], v[182:185]
	v_mfma_f32_16x16x32_f16 v[186:189], v[46:49], v[206:209], v[186:189]
	s_waitcnt lgkmcnt(5)
	ds_read_b128 v[206:209], v243 offset:16656
	v_mfma_f32_16x16x32_f16 v[174:177], v[50:53], v[210:213], v[174:177]
	v_mfma_f32_16x16x32_f16 v[178:181], v[54:57], v[210:213], v[178:181]
	v_mfma_f32_16x16x32_f16 v[182:185], v[58:61], v[210:213], v[182:185]
	v_mfma_f32_16x16x32_f16 v[186:189], v[62:65], v[210:213], v[186:189]
	s_waitcnt lgkmcnt(1)
	ds_read_b128 v[210:213], v242 offset:30064
	v_mfma_f32_16x16x32_f16 v[174:177], v[98:101], v[214:217], v[174:177]
	v_mfma_f32_16x16x32_f16 v[178:181], v[102:105], v[214:217], v[178:181]
	v_mfma_f32_16x16x32_f16 v[182:185], v[106:109], v[214:217], v[182:185]
	v_mfma_f32_16x16x32_f16 v[186:189], v[110:113], v[214:217], v[186:189]
	s_waitcnt lgkmcnt(1)
	ds_read_b128 v[214:217], v242 offset:30016
	v_mfma_f32_16x16x32_f16 v[174:177], v[114:117], v[206:209], v[174:177]
	v_mfma_f32_16x16x32_f16 v[178:181], v[118:121], v[206:209], v[178:181]
	v_mfma_f32_16x16x32_f16 v[182:185], v[122:125], v[206:209], v[182:185]
	v_mfma_f32_16x16x32_f16 v[186:189], v[126:129], v[206:209], v[186:189]
	s_waitcnt lgkmcnt(1)
	ds_read_b128 v[206:209], v242 offset:30032
	v_mfma_f32_16x16x32_f16 v[174:177], v[218:221], v[210:213], v[174:177]
	ds_read_b128 v[218:221], v255 offset:0
	v_mfma_f32_16x16x32_f16 v[178:181], v[222:225], v[210:213], v[178:181]
	ds_read_b128 v[222:225], v255 offset:1024
	v_mfma_f32_16x16x32_f16 v[182:185], v[226:229], v[210:213], v[182:185]
	ds_read_b128 v[226:229], v255 offset:2048
	v_mfma_f32_16x16x32_f16 v[186:189], v[230:233], v[210:213], v[186:189]
	ds_read_b128 v[230:233], v255 offset:3072
	s_waitcnt lgkmcnt(5)
	ds_read_b128 v[210:213], v243 offset:16672
	v_mfma_f32_16x16x32_f16 v[174:177], v[66:69], v[214:217], v[174:177]
	v_mfma_f32_16x16x32_f16 v[178:181], v[70:73], v[214:217], v[178:181]
	v_mfma_f32_16x16x32_f16 v[182:185], v[74:77], v[214:217], v[182:185]
	v_mfma_f32_16x16x32_f16 v[186:189], v[78:81], v[214:217], v[186:189]
	s_waitcnt lgkmcnt(5)
	ds_read_b128 v[214:217], v243 offset:16688
	v_mfma_f32_16x16x32_f16 v[174:177], v[82:85], v[206:209], v[174:177]
	v_mfma_f32_16x16x32_f16 v[178:181], v[86:89], v[206:209], v[178:181]
	v_mfma_f32_16x16x32_f16 v[182:185], v[90:93], v[206:209], v[182:185]
	v_mfma_f32_16x16x32_f16 v[186:189], v[94:97], v[206:209], v[186:189]
	s_waitcnt vmcnt(0)
	ds_write_b128 v249, v[234:237] offset:27648
	ds_write_b128 v249, v[238:241] offset:2304
	global_load_dwordx4 v[234:237], v248, s[8:9]
	s_add_u32 s8, s8, 0x271000
	s_addc_u32 s9, s9, 0
	s_waitcnt lgkmcnt(3)
	ds_read_b128 v[206:209], v242 offset:32256
	v_mfma_f32_16x16x32_f16 v[174:177], v[130:133], v[210:213], v[174:177]
	v_mfma_f32_16x16x32_f16 v[178:181], v[134:137], v[210:213], v[178:181]
	v_mfma_f32_16x16x32_f16 v[182:185], v[138:141], v[210:213], v[182:185]
	v_mfma_f32_16x16x32_f16 v[186:189], v[142:145], v[210:213], v[186:189]
	s_waitcnt lgkmcnt(3)
	ds_read_b128 v[210:213], v242 offset:32272
	v_mfma_f32_16x16x32_f16 v[174:177], v[146:149], v[214:217], v[174:177]
	v_mfma_f32_16x16x32_f16 v[178:181], v[150:153], v[214:217], v[178:181]
	v_mfma_f32_16x16x32_f16 v[182:185], v[154:157], v[214:217], v[182:185]
	v_mfma_f32_16x16x32_f16 v[186:189], v[158:161], v[214:217], v[186:189]
	s_waitcnt lgkmcnt(1)
	ds_read_b128 v[214:217], v242 offset:32352
	v_mfma_f32_16x16x32_f16 v[190:193], v[2:5], v[206:209], v[190:193]
	v_mfma_f32_16x16x32_f16 v[194:197], v[6:9], v[206:209], v[194:197]
	v_mfma_f32_16x16x32_f16 v[198:201], v[10:13], v[206:209], v[198:201]
	v_mfma_f32_16x16x32_f16 v[202:205], v[14:17], v[206:209], v[202:205]
	s_waitcnt lgkmcnt(1)
	ds_read_b128 v[206:209], v242 offset:32288
	v_mfma_f32_16x16x32_f16 v[190:193], v[18:21], v[210:213], v[190:193]
	v_mfma_f32_16x16x32_f16 v[194:197], v[22:25], v[210:213], v[194:197]
	v_mfma_f32_16x16x32_f16 v[198:201], v[26:29], v[210:213], v[198:201]
	v_mfma_f32_16x16x32_f16 v[202:205], v[30:33], v[210:213], v[202:205]
	v_exp_f32_e32 v174, v174
	v_exp_f32_e32 v175, v175
	v_exp_f32_e32 v176, v176
	v_exp_f32_e32 v177, v177
	v_exp_f32_e32 v178, v178
	v_exp_f32_e32 v179, v179
	v_exp_f32_e32 v180, v180
	v_exp_f32_e32 v181, v181
	v_exp_f32_e32 v182, v182
	v_exp_f32_e32 v183, v183
	v_exp_f32_e32 v184, v184
	v_exp_f32_e32 v185, v185
	v_exp_f32_e32 v186, v186
	v_exp_f32_e32 v187, v187
	v_exp_f32_e32 v188, v188
	v_exp_f32_e32 v189, v189
	v_add_f32_e32 v182, 1.0, v182
	v_add_f32_e32 v183, 1.0, v183
	v_add_f32_e32 v184, 1.0, v184
	v_add_f32_e32 v185, 1.0, v185
	v_add_f32_e32 v178, 1.0, v178
	v_add_f32_e32 v179, 1.0, v179
	v_add_f32_e32 v180, 1.0, v180
	v_add_f32_e32 v181, 1.0, v181
	v_fma_f32 v174, v174, v182, v182
	v_fma_f32 v175, v175, v183, v183
	v_fma_f32 v176, v176, v184, v184
	v_fma_f32 v177, v177, v185, v185
	v_rcp_f32_e32 v178, v178
	v_rcp_f32_e32 v179, v179
	v_rcp_f32_e32 v180, v180
	v_rcp_f32_e32 v181, v181
	v_fma_f32 v182, v182, v252, s16
	v_fma_f32 v183, v183, v252, s16
	v_fma_f32 v184, v184, v252, s16
	v_fma_f32 v185, v185, v252, s16
	v_rcp_f32_e32 v174, v174
	v_rcp_f32_e32 v175, v175
	v_rcp_f32_e32 v176, v176
	v_rcp_f32_e32 v177, v177
	v_mul_f32_e32 v166, v166, v178
	v_mul_f32_e32 v167, v167, v179
	v_mul_f32_e32 v168, v168, v180
	v_mul_f32_e32 v169, v169, v181
	v_fma_f32 v166, v182, v174, v166
	v_fma_f32 v167, v183, v175, v167
	v_fma_f32 v168, v184, v176, v168
	v_fma_f32 v169, v185, v177, v169
	v_exp_f32_e32 v178, v166
	v_exp_f32_e32 v179, v167
	v_exp_f32_e32 v180, v168
	v_exp_f32_e32 v181, v169
	v_add_f32_e32 v174, 1.0, v178
	v_add_f32_e32 v175, 1.0, v179
	v_add_f32_e32 v176, 1.0, v180
	v_add_f32_e32 v177, 1.0, v181
	v_add_f32_e32 v182, -1.0, v178
	v_add_f32_e32 v183, -1.0, v179
	v_add_f32_e32 v184, -1.0, v180
	v_add_f32_e32 v185, -1.0, v181
	v_fma_f32 v186, v186, v174, v174
	v_fma_f32 v187, v187, v175, v175
	v_fma_f32 v188, v188, v176, v176
	v_fma_f32 v189, v189, v177, v177
	v_rcp_f32_e32 v186, v186
	v_rcp_f32_e32 v187, v187
	v_rcp_f32_e32 v188, v188
	v_rcp_f32_e32 v189, v189
	v_mul_f32_e32 v186, v182, v186
	v_mul_f32_e32 v187, v183, v187
	v_mul_f32_e32 v188, v184, v188
	v_mul_f32_e32 v189, v185, v189
	v_cvt_pk_f16_f32 v186, v186, v187
	v_cvt_pk_f16_f32 v187, v188, v189
	ds_write_b64 v244, v[186:187] offset:1280
	ds_read_b128 v[174:177], v245 offset:0
	ds_read_b128 v[178:181], v245 offset:512
	ds_read_b128 v[182:185], v245 offset:1024
	ds_read_b128 v[186:189], v245 offset:1536
	s_waitcnt lgkmcnt(6)
	ds_read_b128 v[210:213], v242 offset:32304
	v_mfma_f32_16x16x32_f16 v[190:193], v[218:221], v[214:217], v[190:193]
	ds_read_b128 v[218:221], v255 offset:4096
	v_mfma_f32_16x16x32_f16 v[194:197], v[222:225], v[214:217], v[194:197]
	ds_read_b128 v[222:225], v255 offset:5120
	v_mfma_f32_16x16x32_f16 v[198:201], v[226:229], v[214:217], v[198:201]
	ds_read_b128 v[226:229], v255 offset:6144
	v_mfma_f32_16x16x32_f16 v[202:205], v[230:233], v[214:217], v[202:205]
	ds_read_b128 v[230:233], v255 offset:7168
	s_waitcnt lgkmcnt(10)
	ds_read_b128 v[214:217], v243 offset:17920
	v_mfma_f32_16x16x32_f16 v[190:193], v[34:37], v[206:209], v[190:193]
	v_mfma_f32_16x16x32_f16 v[194:197], v[38:41], v[206:209], v[194:197]
	v_mfma_f32_16x16x32_f16 v[198:201], v[42:45], v[206:209], v[198:201]
	v_mfma_f32_16x16x32_f16 v[202:205], v[46:49], v[206:209], v[202:205]
	s_waitcnt lgkmcnt(5)
	ds_read_b128 v[206:209], v243 offset:17936
	v_mfma_f32_16x16x32_f16 v[190:193], v[50:53], v[210:213], v[190:193]
	v_mfma_f32_16x16x32_f16 v[194:197], v[54:57], v[210:213], v[194:197]
	v_mfma_f32_16x16x32_f16 v[198:201], v[58:61], v[210:213], v[198:201]
	v_mfma_f32_16x16x32_f16 v[202:205], v[62:65], v[210:213], v[202:205]
	s_waitcnt lgkmcnt(1)
	ds_read_b128 v[210:213], v242 offset:32368
	v_mfma_f32_16x16x32_f16 v[190:193], v[98:101], v[214:217], v[190:193]
	v_mfma_f32_16x16x32_f16 v[194:197], v[102:105], v[214:217], v[194:197]
	v_mfma_f32_16x16x32_f16 v[198:201], v[106:109], v[214:217], v[198:201]
	v_mfma_f32_16x16x32_f16 v[202:205], v[110:113], v[214:217], v[202:205]
	s_waitcnt lgkmcnt(1)
	ds_read_b128 v[214:217], v242 offset:32320
	v_mfma_f32_16x16x32_f16 v[190:193], v[114:117], v[206:209], v[190:193]
	v_mfma_f32_16x16x32_f16 v[194:197], v[118:121], v[206:209], v[194:197]
	v_mfma_f32_16x16x32_f16 v[198:201], v[122:125], v[206:209], v[198:201]
	v_mfma_f32_16x16x32_f16 v[202:205], v[126:129], v[206:209], v[202:205]
	s_waitcnt lgkmcnt(1)
	ds_read_b128 v[206:209], v242 offset:32336
	v_mfma_f32_16x16x32_f16 v[190:193], v[218:221], v[210:213], v[190:193]
	ds_read_b128 v[218:221], v255 offset:0
	v_mfma_f32_16x16x32_f16 v[194:197], v[222:225], v[210:213], v[194:197]
	ds_read_b128 v[222:225], v255 offset:1024
	v_mfma_f32_16x16x32_f16 v[198:201], v[226:229], v[210:213], v[198:201]
	ds_read_b128 v[226:229], v255 offset:2048
	v_mfma_f32_16x16x32_f16 v[202:205], v[230:233], v[210:213], v[202:205]
	ds_read_b128 v[230:233], v255 offset:3072
	s_waitcnt lgkmcnt(5)
	ds_read_b128 v[210:213], v243 offset:17952
	v_mfma_f32_16x16x32_f16 v[190:193], v[66:69], v[214:217], v[190:193]
	v_mfma_f32_16x16x32_f16 v[194:197], v[70:73], v[214:217], v[194:197]
	v_mfma_f32_16x16x32_f16 v[198:201], v[74:77], v[214:217], v[198:201]
	v_mfma_f32_16x16x32_f16 v[202:205], v[78:81], v[214:217], v[202:205]
	s_waitcnt lgkmcnt(5)
	ds_read_b128 v[214:217], v243 offset:17968
	v_mfma_f32_16x16x32_f16 v[190:193], v[82:85], v[206:209], v[190:193]
	v_mfma_f32_16x16x32_f16 v[194:197], v[86:89], v[206:209], v[194:197]
	v_mfma_f32_16x16x32_f16 v[198:201], v[90:93], v[206:209], v[198:201]
	v_mfma_f32_16x16x32_f16 v[202:205], v[94:97], v[206:209], v[202:205]
	s_waitcnt lgkmcnt(1)
	ds_read_b128 v[206:209], v242 offset:0
	v_mfma_f32_16x16x32_f16 v[190:193], v[130:133], v[210:213], v[190:193]
	v_mfma_f32_16x16x32_f16 v[194:197], v[134:137], v[210:213], v[194:197]
	v_mfma_f32_16x16x32_f16 v[198:201], v[138:141], v[210:213], v[198:201]
	v_mfma_f32_16x16x32_f16 v[202:205], v[142:145], v[210:213], v[202:205]
	s_waitcnt lgkmcnt(1)
	ds_read_b128 v[210:213], v242 offset:96
	v_mfma_f32_16x16x32_f16 v[190:193], v[146:149], v[214:217], v[190:193]
	v_mfma_f32_16x16x32_f16 v[194:197], v[150:153], v[214:217], v[194:197]
	v_mfma_f32_16x16x32_f16 v[198:201], v[154:157], v[214:217], v[198:201]
	v_mfma_f32_16x16x32_f16 v[202:205], v[158:161], v[214:217], v[202:205]
	s_waitcnt vmcnt(0)
	ds_write_b128 v249, v[234:237] offset:4608
	s_waitcnt lgkmcnt(2)
	ds_read_b128 v[214:217], v242 offset:16
	v_mfma_f32_16x16x32_f16 v[174:177], v[2:5], v[206:209], v[174:177]
	v_mfma_f32_16x16x32_f16 v[178:181], v[6:9], v[206:209], v[178:181]
	v_mfma_f32_16x16x32_f16 v[182:185], v[10:13], v[206:209], v[182:185]
	v_mfma_f32_16x16x32_f16 v[186:189], v[14:17], v[206:209], v[186:189]
	s_waitcnt lgkmcnt(2)
	ds_read_b128 v[206:209], v242 offset:32
	v_mfma_f32_16x16x32_f16 v[174:177], v[218:221], v[210:213], v[174:177]
	ds_read_b128 v[218:221], v255 offset:4096
	v_mfma_f32_16x16x32_f16 v[178:181], v[222:225], v[210:213], v[178:181]
	ds_read_b128 v[222:225], v255 offset:5120
	v_mfma_f32_16x16x32_f16 v[182:185], v[226:229], v[210:213], v[182:185]
	ds_read_b128 v[226:229], v255 offset:6144
	v_mfma_f32_16x16x32_f16 v[186:189], v[230:233], v[210:213], v[186:189]
	ds_read_b128 v[230:233], v255 offset:7168
	v_exp_f32_e32 v190, v190
	v_exp_f32_e32 v191, v191
	v_exp_f32_e32 v192, v192
	v_exp_f32_e32 v193, v193
	v_exp_f32_e32 v194, v194
	v_exp_f32_e32 v195, v195
	v_exp_f32_e32 v196, v196
	v_exp_f32_e32 v197, v197
	v_exp_f32_e32 v198, v198
	v_exp_f32_e32 v199, v199
	v_exp_f32_e32 v200, v200
	v_exp_f32_e32 v201, v201
	v_exp_f32_e32 v202, v202
	v_exp_f32_e32 v203, v203
	v_exp_f32_e32 v204, v204
	v_exp_f32_e32 v205, v205
	v_add_f32_e32 v198, 1.0, v198
	v_add_f32_e32 v199, 1.0, v199
	v_add_f32_e32 v200, 1.0, v200
	v_add_f32_e32 v201, 1.0, v201
	v_add_f32_e32 v194, 1.0, v194
	v_add_f32_e32 v195, 1.0, v195
	v_add_f32_e32 v196, 1.0, v196
	v_add_f32_e32 v197, 1.0, v197
	v_fma_f32 v190, v190, v198, v198
	v_fma_f32 v191, v191, v199, v199
	v_fma_f32 v192, v192, v200, v200
	v_fma_f32 v193, v193, v201, v201
	v_rcp_f32_e32 v194, v194
	v_rcp_f32_e32 v195, v195
	v_rcp_f32_e32 v196, v196
	v_rcp_f32_e32 v197, v197
	v_fma_f32 v198, v198, v252, s16
	v_fma_f32 v199, v199, v252, s16
	v_fma_f32 v200, v200, v252, s16
	v_fma_f32 v201, v201, v252, s16
	v_rcp_f32_e32 v190, v190
	v_rcp_f32_e32 v191, v191
	v_rcp_f32_e32 v192, v192
	v_rcp_f32_e32 v193, v193
	v_mul_f32_e32 v170, v170, v194
	v_mul_f32_e32 v171, v171, v195
	v_mul_f32_e32 v172, v172, v196
	v_mul_f32_e32 v173, v173, v197
	v_fma_f32 v170, v198, v190, v170
	v_fma_f32 v171, v199, v191, v171
	v_fma_f32 v172, v200, v192, v172
	v_fma_f32 v173, v201, v193, v173
	v_exp_f32_e32 v194, v170
	v_exp_f32_e32 v195, v171
	v_exp_f32_e32 v196, v172
	v_exp_f32_e32 v197, v173
	v_add_f32_e32 v190, 1.0, v194
	v_add_f32_e32 v191, 1.0, v195
	v_add_f32_e32 v192, 1.0, v196
	v_add_f32_e32 v193, 1.0, v197
	v_add_f32_e32 v198, -1.0, v194
	v_add_f32_e32 v199, -1.0, v195
	v_add_f32_e32 v200, -1.0, v196
	v_add_f32_e32 v201, -1.0, v197
	v_fma_f32 v202, v202, v190, v190
	v_fma_f32 v203, v203, v191, v191
	v_fma_f32 v204, v204, v192, v192
	v_fma_f32 v205, v205, v193, v193
	v_rcp_f32_e32 v202, v202
	v_rcp_f32_e32 v203, v203
	v_rcp_f32_e32 v204, v204
	v_rcp_f32_e32 v205, v205
	v_mul_f32_e32 v202, v198, v202
	v_mul_f32_e32 v203, v199, v203
	v_mul_f32_e32 v204, v200, v204
	v_mul_f32_e32 v205, v201, v205
	v_cvt_pk_f16_f32 v202, v202, v203
	v_cvt_pk_f16_f32 v203, v204, v205
	ds_write_b64 v244, v[202:203] offset:2560
	ds_read_b128 v[190:193], v245 offset:0
	ds_read_b128 v[194:197], v245 offset:512
	ds_read_b128 v[198:201], v245 offset:1024
	ds_read_b128 v[202:205], v245 offset:1536
	s_waitcnt lgkmcnt(10)
	ds_read_b128 v[210:213], v242 offset:112
	v_mfma_f32_16x16x32_f16 v[174:177], v[18:21], v[214:217], v[174:177]
	v_mfma_f32_16x16x32_f16 v[178:181], v[22:25], v[214:217], v[178:181]
	v_mfma_f32_16x16x32_f16 v[182:185], v[26:29], v[214:217], v[182:185]
	v_mfma_f32_16x16x32_f16 v[186:189], v[30:33], v[214:217], v[186:189]
	s_waitcnt lgkmcnt(10)
	ds_read_b128 v[214:217], v242 offset:48
	v_mfma_f32_16x16x32_f16 v[174:177], v[34:37], v[206:209], v[174:177]
	v_mfma_f32_16x16x32_f16 v[178:181], v[38:41], v[206:209], v[178:181]
	v_mfma_f32_16x16x32_f16 v[182:185], v[42:45], v[206:209], v[182:185]
	v_mfma_f32_16x16x32_f16 v[186:189], v[46:49], v[206:209], v[186:189]
	s_waitcnt lgkmcnt(1)
	ds_read_b128 v[206:209], v242 offset:64
	v_mfma_f32_16x16x32_f16 v[174:177], v[218:221], v[210:213], v[174:177]
	ds_read_b128 v[218:221], v255 offset:0
	v_mfma_f32_16x16x32_f16 v[178:181], v[222:225], v[210:213], v[178:181]
	ds_read_b128 v[222:225], v255 offset:1024
	v_mfma_f32_16x16x32_f16 v[182:185], v[226:229], v[210:213], v[182:185]
	ds_read_b128 v[226:229], v255 offset:2048
	v_mfma_f32_16x16x32_f16 v[186:189], v[230:233], v[210:213], v[186:189]
	ds_read_b128 v[230:233], v255 offset:3072
	s_waitcnt lgkmcnt(5)
	ds_read_b128 v[210:213], v242 offset:80
	v_mfma_f32_16x16x32_f16 v[174:177], v[50:53], v[214:217], v[174:177]
	v_mfma_f32_16x16x32_f16 v[178:181], v[54:57], v[214:217], v[178:181]
	v_mfma_f32_16x16x32_f16 v[182:185], v[58:61], v[214:217], v[182:185]
	v_mfma_f32_16x16x32_f16 v[186:189], v[62:65], v[214:217], v[186:189]
	s_waitcnt lgkmcnt(0)
	s_barrier
	s_add_u32 s17, s17, 2
	s_cmp_lt_u32 s17, 16
	s_cbranch_scc1 .Llstm1_loop
	s_waitcnt lgkmcnt(0)
	ds_read_b128 v[234:237], v250
	s_mov_b64 exec, s[20:21]
	ds_read_b128 v[238:241], v250 offset:2560
	s_mov_b64 exec, -1
	s_waitcnt lgkmcnt(0)
	s_mov_b64 exec, s[18:19]
	global_store_dwordx4 v251, v[234:237], s[10:11]
	s_mov_b64 exec, s[20:21]
	global_store_dwordx4 v251, v[238:241], s[14:15]
	s_mov_b64 exec, -1
	s_branch .LBB6_39

.Lskipx51:
	s_waitcnt lgkmcnt(1)
	ds_read_b128 v[174:177], v195 offset:32
	v_mfma_f32_16x16x32_f16 v[142:145], v[66:69], v[178:181], v[142:145]
	v_mfma_f32_16x16x32_f16 v[146:149], v[70:73], v[178:181], v[146:149]
	v_mfma_f32_16x16x32_f16 v[150:153], v[74:77], v[178:181], v[150:153]
	v_mfma_f32_16x16x32_f16 v[154:157], v[78:81], v[178:181], v[154:157]
	global_load_dwordx4 v[190:193], v199, s[8:9]
	s_waitcnt lgkmcnt(1)
	ds_read_b128 v[178:181], v195 offset:48
	v_mfma_f32_16x16x32_f16 v[142:145], v[82:85], v[182:185], v[142:145]
	v_mfma_f32_16x16x32_f16 v[146:149], v[86:89], v[182:185], v[146:149]
	v_mfma_f32_16x16x32_f16 v[150:153], v[90:93], v[182:185], v[150:153]
	v_mfma_f32_16x16x32_f16 v[154:157], v[94:97], v[182:185], v[154:157]
	s_add_u32 s12, s12, 0x271000
	s_waitcnt lgkmcnt(1)
	ds_read_b128 v[182:185], v194 offset:1280
	v_mfma_f32_16x16x32_f16 v[142:145], v[98:101], v[174:177], v[142:145]
	v_mfma_f32_16x16x32_f16 v[146:149], v[102:105], v[174:177], v[146:149]
	v_mfma_f32_16x16x32_f16 v[150:153], v[106:109], v[174:177], v[150:153]
	v_mfma_f32_16x16x32_f16 v[154:157], v[110:113], v[174:177], v[154:157]
	s_addc_u32 s13, s13, 0
	s_waitcnt lgkmcnt(1)
	ds_read_b128 v[174:177], v194 offset:1296
	v_mfma_f32_16x16x32_f16 v[142:145], v[114:117], v[178:181], v[142:145]
	v_mfma_f32_16x16x32_f16 v[146:149], v[118:121], v[178:181], v[146:149]
	s_add_u32 s8, s8, 0x271000
	v_mfma_f32_16x16x32_f16 v[150:153], v[122:125], v[178:181], v[150:153]
	v_mfma_f32_16x16x32_f16 v[154:157], v[126:129], v[178:181], v[154:157]
	s_addc_u32 s9, s9, 0
	s_waitcnt lgkmcnt(1)
	ds_read_b128 v[178:181], v195 offset:1280
	v_mfma_f32_16x16x32_f16 v[158:161], v[2:5], v[182:185], v[158:161]
	v_mfma_f32_16x16x32_f16 v[162:165], v[6:9], v[182:185], v[162:165]
	v_mfma_f32_16x16x32_f16 v[166:169], v[10:13], v[182:185], v[166:169]
	v_mfma_f32_16x16x32_f16 v[170:173], v[14:17], v[182:185], v[170:173]
	s_waitcnt lgkmcnt(1)
	ds_read_b128 v[182:185], v195 offset:1296
	v_mfma_f32_16x16x32_f16 v[158:161], v[18:21], v[174:177], v[158:161]
	v_mfma_f32_16x16x32_f16 v[162:165], v[22:25], v[174:177], v[162:165]
	v_mfma_f32_16x16x32_f16 v[166:169], v[26:29], v[174:177], v[166:169]
	v_mfma_f32_16x16x32_f16 v[170:173], v[30:33], v[174:177], v[170:173]
	v_exp_f32_e32 v142, v142
	v_exp_f32_e32 v143, v143
	v_exp_f32_e32 v144, v144
	v_exp_f32_e32 v145, v145
	v_exp_f32_e32 v146, v146
	v_exp_f32_e32 v147, v147
	v_exp_f32_e32 v148, v148
	v_exp_f32_e32 v149, v149
	v_exp_f32_e32 v150, v150
	v_exp_f32_e32 v151, v151
	v_exp_f32_e32 v152, v152
	v_exp_f32_e32 v153, v153
	v_exp_f32_e32 v154, v154
	v_exp_f32_e32 v155, v155
	v_exp_f32_e32 v156, v156
	v_exp_f32_e32 v157, v157
	v_add_f32_e32 v150, 1.0, v150
	v_add_f32_e32 v151, 1.0, v151
	v_add_f32_e32 v152, 1.0, v152
	v_add_f32_e32 v153, 1.0, v153
	v_add_f32_e32 v146, 1.0, v146
	v_add_f32_e32 v147, 1.0, v147
	v_add_f32_e32 v148, 1.0, v148
	v_add_f32_e32 v149, 1.0, v149
	v_fma_f32 v142, v142, v150, v150
	v_fma_f32 v143, v143, v151, v151
	v_fma_f32 v144, v144, v152, v152
	v_fma_f32 v145, v145, v153, v153
	v_rcp_f32_e32 v146, v146
	v_rcp_f32_e32 v147, v147
	v_rcp_f32_e32 v148, v148
	v_rcp_f32_e32 v149, v149
	v_fma_f32 v150, v150, v204, s16
	v_fma_f32 v151, v151, v204, s16
	v_fma_f32 v152, v152, v204, s16
	v_fma_f32 v153, v153, v204, s16
	v_rcp_f32_e32 v142, v142
	v_rcp_f32_e32 v143, v143
	v_rcp_f32_e32 v144, v144
	v_rcp_f32_e32 v145, v145
	v_mul_f32_e32 v130, v130, v146
	v_mul_f32_e32 v131, v131, v147
	v_mul_f32_e32 v132, v132, v148
	v_mul_f32_e32 v133, v133, v149
	v_fma_f32 v130, v150, v142, v130
	v_fma_f32 v131, v151, v143, v131
	v_fma_f32 v132, v152, v144, v132
	v_fma_f32 v133, v153, v145, v133
	v_exp_f32_e32 v146, v130
	v_exp_f32_e32 v147, v131
	v_exp_f32_e32 v148, v132
	v_exp_f32_e32 v149, v133
	v_add_f32_e32 v142, 1.0, v146
	v_add_f32_e32 v143, 1.0, v147
	v_add_f32_e32 v144, 1.0, v148
	v_add_f32_e32 v145, 1.0, v149
	v_add_f32_e32 v150, -1.0, v146
	v_add_f32_e32 v151, -1.0, v147
	v_add_f32_e32 v152, -1.0, v148
	v_add_f32_e32 v153, -1.0, v149
	v_fma_f32 v154, v154, v142, v142
	v_fma_f32 v155, v155, v143, v143
	v_fma_f32 v156, v156, v144, v144
	v_fma_f32 v157, v157, v145, v145
	v_rcp_f32_e32 v154, v154
	v_rcp_f32_e32 v155, v155
	v_rcp_f32_e32 v156, v156
	v_rcp_f32_e32 v157, v157
	v_mul_f32_e32 v154, v150, v154
	v_mul_f32_e32 v155, v151, v155
	v_mul_f32_e32 v156, v152, v156
	v_mul_f32_e32 v157, v153, v157
	v_cvt_pk_f16_f32 v154, v154, v155
	v_cvt_pk_f16_f32 v155, v156, v157
	ds_write_b64 v196, v[154:155] offset:15360
	ds_read_b128 v[142:145], v197 offset:0
	ds_read_b128 v[146:149], v197 offset:512
	ds_read_b128 v[150:153], v197 offset:1024
	ds_read_b128 v[154:157], v197 offset:1536
	s_waitcnt lgkmcnt(6)
	ds_read_b128 v[174:177], v194 offset:1312
	v_mfma_f32_16x16x32_f16 v[158:161], v[66:69], v[178:181], v[158:161]
	v_mfma_f32_16x16x32_f16 v[162:165], v[70:73], v[178:181], v[162:165]
	v_mfma_f32_16x16x32_f16 v[166:169], v[74:77], v[178:181], v[166:169]
	v_mfma_f32_16x16x32_f16 v[170:173], v[78:81], v[178:181], v[170:173]
	s_waitcnt lgkmcnt(6)
	ds_read_b128 v[178:181], v194 offset:1328
	v_mfma_f32_16x16x32_f16 v[158:161], v[82:85], v[182:185], v[158:161]
	v_mfma_f32_16x16x32_f16 v[162:165], v[86:89], v[182:185], v[162:165]
	v_mfma_f32_16x16x32_f16 v[166:169], v[90:93], v[182:185], v[166:169]
	v_mfma_f32_16x16x32_f16 v[170:173], v[94:97], v[182:185], v[170:173]
	s_waitcnt lgkmcnt(1)
	ds_read_b128 v[182:185], v195 offset:1312
	v_mfma_f32_16x16x32_f16 v[158:161], v[34:37], v[174:177], v[158:161]
	v_mfma_f32_16x16x32_f16 v[162:165], v[38:41], v[174:177], v[162:165]
	v_mfma_f32_16x16x32_f16 v[166:169], v[42:45], v[174:177], v[166:169]
	v_mfma_f32_16x16x32_f16 v[170:173], v[46:49], v[174:177], v[170:173]
	s_waitcnt lgkmcnt(1)
	ds_read_b128 v[174:177], v195 offset:1328
	v_mfma_f32_16x16x32_f16 v[158:161], v[50:53], v[178:181], v[158:161]
	v_mfma_f32_16x16x32_f16 v[162:165], v[54:57], v[178:181], v[162:165]
	v_mfma_f32_16x16x32_f16 v[166:169], v[58:61], v[178:181], v[166:169]
	v_mfma_f32_16x16x32_f16 v[170:173], v[62:65], v[178:181], v[170:173]
	s_waitcnt vmcnt(0)
	s_cmp_ge_u32 s24, 4
	s_cbranch_scc1 .Lskips52
	ds_write_b128 v201, v[186:189] offset:0
.Lskips52:
	ds_write_b128 v201, v[190:193] offset:16640
	s_waitcnt lgkmcnt(3)
	ds_read_b128 v[178:181], v194 offset:2560
	v_mfma_f32_16x16x32_f16 v[158:161], v[98:101], v[182:185], v[158:161]
	v_mfma_f32_16x16x32_f16 v[162:165], v[102:105], v[182:185], v[162:165]
	v_mfma_f32_16x16x32_f16 v[166:169], v[106:109], v[182:185], v[166:169]
	v_mfma_f32_16x16x32_f16 v[170:173], v[110:113], v[182:185], v[170:173]
	s_waitcnt lgkmcnt(3)
	ds_read_b128 v[182:185], v194 offset:2576
	v_mfma_f32_16x16x32_f16 v[158:161], v[114:117], v[174:177], v[158:161]
	v_mfma_f32_16x16x32_f16 v[162:165], v[118:121], v[174:177], v[162:165]
	v_mfma_f32_16x16x32_f16 v[166:169], v[122:125], v[174:177], v[166:169]
	v_mfma_f32_16x16x32_f16 v[170:173], v[126:129], v[174:177], v[170:173]
	s_waitcnt lgkmcnt(1)
	ds_read_b128 v[174:177], v195 offset:2560
	v_mfma_f32_16x16x32_f16 v[142:145], v[2:5], v[178:181], v[142:145]
	v_mfma_f32_16x16x32_f16 v[146:149], v[6:9], v[178:181], v[146:149]
	v_mfma_f32_16x16x32_f16 v[150:153], v[10:13], v[178:181], v[150:153]
	v_mfma_f32_16x16x32_f16 v[154:157], v[14:17], v[178:181], v[154:157]
	s_waitcnt lgkmcnt(1)
	ds_read_b128 v[178:181], v195 offset:2576
	v_mfma_f32_16x16x32_f16 v[142:145], v[18:21], v[182:185], v[142:145]
	v_mfma_f32_16x16x32_f16 v[146:149], v[22:25], v[182:185], v[146:149]
	v_mfma_f32_16x16x32_f16 v[150:153], v[26:29], v[182:185], v[150:153]
	v_mfma_f32_16x16x32_f16 v[154:157], v[30:33], v[182:185], v[154:157]
	v_exp_f32_e32 v158, v158
	v_exp_f32_e32 v159, v159
	v_exp_f32_e32 v160, v160
	v_exp_f32_e32 v161, v161
	v_exp_f32_e32 v162, v162
	v_exp_f32_e32 v163, v163
	v_exp_f32_e32 v164, v164
	v_exp_f32_e32 v165, v165
	v_exp_f32_e32 v166, v166
	v_exp_f32_e32 v167, v167
	v_exp_f32_e32 v168, v168
	v_exp_f32_e32 v169, v169
	v_exp_f32_e32 v170, v170
	v_exp_f32_e32 v171, v171
	v_exp_f32_e32 v172, v172
	v_exp_f32_e32 v173, v173
	v_add_f32_e32 v166, 1.0, v166
	v_add_f32_e32 v167, 1.0, v167
	v_add_f32_e32 v168, 1.0, v168
	v_add_f32_e32 v169, 1.0, v169
	v_add_f32_e32 v162, 1.0, v162
	v_add_f32_e32 v163, 1.0, v163
	v_add_f32_e32 v164, 1.0, v164
	v_add_f32_e32 v165, 1.0, v165
	v_fma_f32 v158, v158, v166, v166
	v_fma_f32 v159, v159, v167, v167
	v_fma_f32 v160, v160, v168, v168
	v_fma_f32 v161, v161, v169, v169
	v_rcp_f32_e32 v162, v162
	v_rcp_f32_e32 v163, v163
	v_rcp_f32_e32 v164, v164
	v_rcp_f32_e32 v165, v165
	v_fma_f32 v166, v166, v204, s16
	v_fma_f32 v167, v167, v204, s16
	v_fma_f32 v168, v168, v204, s16
	v_fma_f32 v169, v169, v204, s16
	v_rcp_f32_e32 v158, v158
	v_rcp_f32_e32 v159, v159
	v_rcp_f32_e32 v160, v160
	v_rcp_f32_e32 v161, v161
	v_mul_f32_e32 v134, v134, v162
	v_mul_f32_e32 v135, v135, v163
	v_mul_f32_e32 v136, v136, v164
	v_mul_f32_e32 v137, v137, v165
	v_fma_f32 v134, v166, v158, v134
	v_fma_f32 v135, v167, v159, v135
	v_fma_f32 v136, v168, v160, v136
	v_fma_f32 v137, v169, v161, v137
	v_exp_f32_e32 v162, v134
	v_exp_f32_e32 v163, v135
	v_exp_f32_e32 v164, v136
	v_exp_f32_e32 v165, v137
	v_add_f32_e32 v158, 1.0, v162
	v_add_f32_e32 v159, 1.0, v163
	v_add_f32_e32 v160, 1.0, v164
	v_add_f32_e32 v161, 1.0, v165
	v_add_f32_e32 v166, -1.0, v162
	v_add_f32_e32 v167, -1.0, v163
	v_add_f32_e32 v168, -1.0, v164
	v_add_f32_e32 v169, -1.0, v165
	v_fma_f32 v170, v170, v158, v158
	v_fma_f32 v171, v171, v159, v159
	v_fma_f32 v172, v172, v160, v160
	v_fma_f32 v173, v173, v161, v161
	v_rcp_f32_e32 v170, v170
	v_rcp_f32_e32 v171, v171
	v_rcp_f32_e32 v172, v172
	v_rcp_f32_e32 v173, v173
	v_mul_f32_e32 v170, v166, v170
	v_mul_f32_e32 v171, v167, v171
	v_mul_f32_e32 v172, v168, v172
	v_mul_f32_e32 v173, v169, v173
	v_cvt_pk_f16_f32 v170, v170, v171
	v_cvt_pk_f16_f32 v171, v172, v173
	ds_write_b64 v196, v[170:171] offset:16640
	ds_read_b128 v[158:161], v197 offset:0
	ds_read_b128 v[162:165], v197 offset:512
	ds_read_b128 v[166:169], v197 offset:1024
	ds_read_b128 v[170:173], v197 offset:1536
	s_waitcnt lgkmcnt(6)
	ds_read_b128 v[182:185], v194 offset:2592
	v_mfma_f32_16x16x32_f16 v[142:145], v[66:69], v[174:177], v[142:145]
	v_mfma_f32_16x16x32_f16 v[146:149], v[70:73], v[174:177], v[146:149]
	v_mfma_f32_16x16x32_f16 v[150:153], v[74:77], v[174:177], v[150:153]
	v_mfma_f32_16x16x32_f16 v[154:157], v[78:81], v[174:177], v[154:157]
	s_waitcnt lgkmcnt(6)
	ds_read_b128 v[174:177], v194 offset:2608
	v_mfma_f32_16x16x32_f16 v[142:145], v[82:85], v[178:181], v[142:145]
	v_mfma_f32_16x16x32_f16 v[146:149], v[86:89], v[178:181], v[146:149]
	v_mfma_f32_16x16x32_f16 v[150:153], v[90:93], v[178:181], v[150:153]
	v_mfma_f32_16x16x32_f16 v[154:157], v[94:97], v[178:181], v[154:157]
	s_waitcnt lgkmcnt(1)
	ds_read_b128 v[178:181], v195 offset:2592
	v_mfma_f32_16x16x32_f16 v[142:145], v[34:37], v[182:185], v[142:145]
	v_mfma_f32_16x16x32_f16 v[146:149], v[38:41], v[182:185], v[146:149]
	v_mfma_f32_16x16x32_f16 v[150:153], v[42:45], v[182:185], v[150:153]
	v_mfma_f32_16x16x32_f16 v[154:157], v[46:49], v[182:185], v[154:157]
	s_waitcnt lgkmcnt(1)
	ds_read_b128 v[182:185], v195 offset:2608
	v_mfma_f32_16x16x32_f16 v[142:145], v[50:53], v[174:177], v[142:145]
	v_mfma_f32_16x16x32_f16 v[146:149], v[54:57], v[174:177], v[146:149]
	v_mfma_f32_16x16x32_f16 v[150:153], v[58:61], v[174:177], v[150:153]
	v_mfma_f32_16x16x32_f16 v[154:157], v[62:65], v[174:177], v[154:157]
	s_waitcnt lgkmcnt(1)
	ds_read_b128 v[174:177], v194 offset:15360
	v_mfma_f32_16x16x32_f16 v[142:145], v[98:101], v[178:181], v[142:145]
	v_mfma_f32_16x16x32_f16 v[146:149], v[102:105], v[178:181], v[146:149]
	v_mfma_f32_16x16x32_f16 v[150:153], v[106:109], v[178:181], v[150:153]
	v_mfma_f32_16x16x32_f16 v[154:157], v[110:113], v[178:181], v[154:157]
	s_waitcnt lgkmcnt(1)
	ds_read_b128 v[178:181], v194 offset:15376
	v_mfma_f32_16x16x32_f16 v[142:145], v[114:117], v[182:185], v[142:145]
	v_mfma_f32_16x16x32_f16 v[146:149], v[118:121], v[182:185], v[146:149]
	v_mfma_f32_16x16x32_f16 v[150:153], v[122:125], v[182:185], v[150:153]
	v_mfma_f32_16x16x32_f16 v[154:157], v[126:129], v[182:185], v[154:157]
	s_waitcnt lgkmcnt(1)
	ds_read_b128 v[182:185], v194 offset:15392
	v_mfma_f32_16x16x32_f16 v[158:161], v[2:5], v[174:177], v[158:161]
	v_mfma_f32_16x16x32_f16 v[162:165], v[6:9], v[174:177], v[162:165]
	v_mfma_f32_16x16x32_f16 v[166:169], v[10:13], v[174:177], v[166:169]
	v_mfma_f32_16x16x32_f16 v[170:173], v[14:17], v[174:177], v[170:173]
	s_waitcnt lgkmcnt(1)
	ds_read_b128 v[174:177], v194 offset:15408
	v_mfma_f32_16x16x32_f16 v[158:161], v[18:21], v[178:181], v[158:161]
	v_mfma_f32_16x16x32_f16 v[162:165], v[22:25], v[178:181], v[162:165]
	v_mfma_f32_16x16x32_f16 v[166:169], v[26:29], v[178:181], v[166:169]
	v_mfma_f32_16x16x32_f16 v[170:173], v[30:33], v[178:181], v[170:173]
	v_exp_f32_e32 v142, v142
	v_exp_f32_e32 v143, v143
	v_exp_f32_e32 v144, v144
	v_exp_f32_e32 v145, v145
	v_exp_f32_e32 v146, v146
	v_exp_f32_e32 v147, v147
	v_exp_f32_e32 v148, v148
	v_exp_f32_e32 v149, v149
	v_exp_f32_e32 v150, v150
	v_exp_f32_e32 v151, v151
	v_exp_f32_e32 v152, v152
	v_exp_f32_e32 v153, v153
	v_exp_f32_e32 v154, v154
	v_exp_f32_e32 v155, v155
	v_exp_f32_e32 v156, v156
	v_exp_f32_e32 v157, v157
	v_add_f32_e32 v150, 1.0, v150
	v_add_f32_e32 v151, 1.0, v151
	v_add_f32_e32 v152, 1.0, v152
	v_add_f32_e32 v153, 1.0, v153
	v_add_f32_e32 v146, 1.0, v146
	v_add_f32_e32 v147, 1.0, v147
	v_add_f32_e32 v148, 1.0, v148
	v_add_f32_e32 v149, 1.0, v149
	v_fma_f32 v142, v142, v150, v150
	v_fma_f32 v143, v143, v151, v151
	v_fma_f32 v144, v144, v152, v152
	v_fma_f32 v145, v145, v153, v153
	v_rcp_f32_e32 v146, v146
	v_rcp_f32_e32 v147, v147
	v_rcp_f32_e32 v148, v148
	v_rcp_f32_e32 v149, v149
	v_fma_f32 v150, v150, v204, s16
	v_fma_f32 v151, v151, v204, s16
	v_fma_f32 v152, v152, v204, s16
	v_fma_f32 v153, v153, v204, s16
	v_rcp_f32_e32 v142, v142
	v_rcp_f32_e32 v143, v143
	v_rcp_f32_e32 v144, v144
	v_rcp_f32_e32 v145, v145
	v_mul_f32_e32 v138, v138, v146
	v_mul_f32_e32 v139, v139, v147
	v_mul_f32_e32 v140, v140, v148
	v_mul_f32_e32 v141, v141, v149
	v_fma_f32 v138, v150, v142, v138
	v_fma_f32 v139, v151, v143, v139
	v_fma_f32 v140, v152, v144, v140
	v_fma_f32 v141, v153, v145, v141
	v_exp_f32_e32 v146, v138
	v_exp_f32_e32 v147, v139
	v_exp_f32_e32 v148, v140
	v_exp_f32_e32 v149, v141
	v_add_f32_e32 v142, 1.0, v146
	v_add_f32_e32 v143, 1.0, v147
	v_add_f32_e32 v144, 1.0, v148
	v_add_f32_e32 v145, 1.0, v149
	v_add_f32_e32 v150, -1.0, v146
	v_add_f32_e32 v151, -1.0, v147
	v_add_f32_e32 v152, -1.0, v148
	v_add_f32_e32 v153, -1.0, v149
	v_fma_f32 v154, v154, v142, v142
	v_fma_f32 v155, v155, v143, v143
	v_fma_f32 v156, v156, v144, v144
	v_fma_f32 v157, v157, v145, v145
	v_rcp_f32_e32 v154, v154
	v_rcp_f32_e32 v155, v155
	v_rcp_f32_e32 v156, v156
	v_rcp_f32_e32 v157, v157
	v_mul_f32_e32 v154, v150, v154
	v_mul_f32_e32 v155, v151, v155
	v_mul_f32_e32 v156, v152, v156
	v_mul_f32_e32 v157, v153, v157
	v_cvt_pk_f16_f32 v154, v154, v155
	v_cvt_pk_f16_f32 v155, v156, v157
	ds_write_b64 v196, v[154:155] offset:17920
	ds_read_b128 v[142:145], v197 offset:0
	ds_read_b128 v[146:149], v197 offset:512
	ds_read_b128 v[150:153], v197 offset:1024
	ds_read_b128 v[154:157], v197 offset:1536
	s_waitcnt lgkmcnt(0)
	s_barrier
	ds_read_b128 v[178:181], v195 offset:15360
	v_mfma_f32_16x16x32_f16 v[158:161], v[34:37], v[182:185], v[158:161]
	v_mfma_f32_16x16x32_f16 v[162:165], v[38:41], v[182:185], v[162:165]
	v_mfma_f32_16x16x32_f16 v[166:169], v[42:45], v[182:185], v[166:169]
	v_mfma_f32_16x16x32_f16 v[170:173], v[46:49], v[182:185], v[170:173]
	ds_read_b128 v[182:185], v195 offset:15376
	v_mfma_f32_16x16x32_f16 v[158:161], v[50:53], v[174:177], v[158:161]
	v_mfma_f32_16x16x32_f16 v[162:165], v[54:57], v[174:177], v[162:165]
	v_mfma_f32_16x16x32_f16 v[166:169], v[58:61], v[174:177], v[166:169]
	v_mfma_f32_16x16x32_f16 v[170:173], v[62:65], v[174:177], v[170:173]
	s_cmp_ge_u32 s24, 4
	s_cbranch_scc1 .Lskipx84
	s_cmp_eq_u32 s17, 14
	s_cbranch_scc1 .Lskipx84
	global_load_dwordx4 v[186:189], v198, s[12:13]
.Lskipx84:
	s_waitcnt lgkmcnt(1)
	ds_read_b128 v[174:177], v195 offset:15392
	v_mfma_f32_16x16x32_f16 v[158:161], v[66:69], v[178:181], v[158:161]
	v_mfma_f32_16x16x32_f16 v[162:165], v[70:73], v[178:181], v[162:165]
	v_mfma_f32_16x16x32_f16 v[166:169], v[74:77], v[178:181], v[166:169]
	v_mfma_f32_16x16x32_f16 v[170:173], v[78:81], v[178:181], v[170:173]
	global_load_dwordx4 v[190:193], v199, s[8:9]
	s_waitcnt lgkmcnt(1)
	ds_read_b128 v[178:181], v195 offset:15408
	v_mfma_f32_16x16x32_f16 v[158:161], v[82:85], v[182:185], v[158:161]
	v_mfma_f32_16x16x32_f16 v[162:165], v[86:89], v[182:185], v[162:165]
	v_mfma_f32_16x16x32_f16 v[166:169], v[90:93], v[182:185], v[166:169]
	v_mfma_f32_16x16x32_f16 v[170:173], v[94:97], v[182:185], v[170:173]
	s_add_u32 s12, s12, 0x271000
	s_waitcnt lgkmcnt(1)
	ds_read_b128 v[182:185], v194 offset:16640
	v_mfma_f32_16x16x32_f16 v[158:161], v[98:101], v[174:177], v[158:161]
	v_mfma_f32_16x16x32_f16 v[162:165], v[102:105], v[174:177], v[162:165]
	v_mfma_f32_16x16x32_f16 v[166:169], v[106:109], v[174:177], v[166:169]
	v_mfma_f32_16x16x32_f16 v[170:173], v[110:113], v[174:177], v[170:173]
	s_addc_u32 s13, s13, 0
	s_waitcnt lgkmcnt(1)
	ds_read_b128 v[174:177], v194 offset:16656
	v_mfma_f32_16x16x32_f16 v[158:161], v[114:117], v[178:181], v[158:161]
	v_mfma_f32_16x16x32_f16 v[162:165], v[118:121], v[178:181], v[162:165]
	s_add_u32 s8, s8, 0x271000
	v_mfma_f32_16x16x32_f16 v[166:169], v[122:125], v[178:181], v[166:169]
	v_mfma_f32_16x16x32_f16 v[170:173], v[126:129], v[178:181], v[170:173]
	s_addc_u32 s9, s9, 0
	s_waitcnt lgkmcnt(1)
	ds_read_b128 v[178:181], v195 offset:16640
	v_mfma_f32_16x16x32_f16 v[142:145], v[2:5], v[182:185], v[142:145]
	v_mfma_f32_16x16x32_f16 v[146:149], v[6:9], v[182:185], v[146:149]
	v_mfma_f32_16x16x32_f16 v[150:153], v[10:13], v[182:185], v[150:153]
	v_mfma_f32_16x16x32_f16 v[154:157], v[14:17], v[182:185], v[154:157]
	s_waitcnt lgkmcnt(1)
	ds_read_b128 v[182:185], v195 offset:16656
	v_mfma_f32_16x16x32_f16 v[142:145], v[18:21], v[174:177], v[142:145]
	v_mfma_f32_16x16x32_f16 v[146:149], v[22:25], v[174:177], v[146:149]
	v_mfma_f32_16x16x32_f16 v[150:153], v[26:29], v[174:177], v[150:153]
	v_mfma_f32_16x16x32_f16 v[154:157], v[30:33], v[174:177], v[154:157]
	v_exp_f32_e32 v158, v158
	v_exp_f32_e32 v159, v159
	v_exp_f32_e32 v160, v160
	v_exp_f32_e32 v161, v161
	v_exp_f32_e32 v162, v162
	v_exp_f32_e32 v163, v163
	v_exp_f32_e32 v164, v164
	v_exp_f32_e32 v165, v165
	v_exp_f32_e32 v166, v166
	v_exp_f32_e32 v167, v167
	v_exp_f32_e32 v168, v168
	v_exp_f32_e32 v169, v169
	v_exp_f32_e32 v170, v170
	v_exp_f32_e32 v171, v171
	v_exp_f32_e32 v172, v172
	v_exp_f32_e32 v173, v173
	v_add_f32_e32 v166, 1.0, v166
	v_add_f32_e32 v167, 1.0, v167
	v_add_f32_e32 v168, 1.0, v168
	v_add_f32_e32 v169, 1.0, v169
	v_add_f32_e32 v162, 1.0, v162
	v_add_f32_e32 v163, 1.0, v163
	v_add_f32_e32 v164, 1.0, v164
	v_add_f32_e32 v165, 1.0, v165
	v_fma_f32 v158, v158, v166, v166
	v_fma_f32 v159, v159, v167, v167
	v_fma_f32 v160, v160, v168, v168
	v_fma_f32 v161, v161, v169, v169
	v_rcp_f32_e32 v162, v162
	v_rcp_f32_e32 v163, v163
	v_rcp_f32_e32 v164, v164
	v_rcp_f32_e32 v165, v165
	v_fma_f32 v166, v166, v204, s16
	v_fma_f32 v167, v167, v204, s16
	v_fma_f32 v168, v168, v204, s16
	v_fma_f32 v169, v169, v204, s16
	v_rcp_f32_e32 v158, v158
	v_rcp_f32_e32 v159, v159
	v_rcp_f32_e32 v160, v160
	v_rcp_f32_e32 v161, v161
	v_mul_f32_e32 v130, v130, v162
	v_mul_f32_e32 v131, v131, v163
	v_mul_f32_e32 v132, v132, v164
	v_mul_f32_e32 v133, v133, v165
	v_fma_f32 v130, v166, v158, v130
	v_fma_f32 v131, v167, v159, v131
	v_fma_f32 v132, v168, v160, v132
	v_fma_f32 v133, v169, v161, v133
	v_exp_f32_e32 v162, v130
	v_exp_f32_e32 v163, v131
	v_exp_f32_e32 v164, v132
	v_exp_f32_e32 v165, v133
	v_add_f32_e32 v158, 1.0, v162
	v_add_f32_e32 v159, 1.0, v163
	v_add_f32_e32 v160, 1.0, v164
	v_add_f32_e32 v161, 1.0, v165
	v_add_f32_e32 v166, -1.0, v162
	v_add_f32_e32 v167, -1.0, v163
	v_add_f32_e32 v168, -1.0, v164
	v_add_f32_e32 v169, -1.0, v165
	v_fma_f32 v170, v170, v158, v158
	v_fma_f32 v171, v171, v159, v159
	v_fma_f32 v172, v172, v160, v160
	v_fma_f32 v173, v173, v161, v161
	v_rcp_f32_e32 v170, v170
	v_rcp_f32_e32 v171, v171
	v_rcp_f32_e32 v172, v172
	v_rcp_f32_e32 v173, v173
	v_mul_f32_e32 v170, v166, v170
	v_mul_f32_e32 v171, v167, v171
	v_mul_f32_e32 v172, v168, v172
	v_mul_f32_e32 v173, v169, v173
	v_cvt_pk_f16_f32 v170, v170, v171
	v_cvt_pk_f16_f32 v171, v172, v173
	ds_write_b64 v196, v[170:171] offset:0
	ds_read_b128 v[158:161], v197 offset:0
	ds_read_b128 v[162:165], v197 offset:512
	ds_read_b128 v[166:169], v197 offset:1024
	ds_read_b128 v[170:173], v197 offset:1536
	s_waitcnt lgkmcnt(6)
	ds_read_b128 v[174:177], v194 offset:16672
	v_mfma_f32_16x16x32_f16 v[142:145], v[66:69], v[178:181], v[142:145]
	v_mfma_f32_16x16x32_f16 v[146:149], v[70:73], v[178:181], v[146:149]
	v_mfma_f32_16x16x32_f16 v[150:153], v[74:77], v[178:181], v[150:153]
	v_mfma_f32_16x16x32_f16 v[154:157], v[78:81], v[178:181], v[154:157]
	s_waitcnt lgkmcnt(6)
	ds_read_b128 v[178:181], v194 offset:16688
	v_mfma_f32_16x16x32_f16 v[142:145], v[82:85], v[182:185], v[142:145]
	v_mfma_f32_16x16x32_f16 v[146:149], v[86:89], v[182:185], v[146:149]
	v_mfma_f32_16x16x32_f16 v[150:153], v[90:93], v[182:185], v[150:153]
	v_mfma_f32_16x16x32_f16 v[154:157], v[94:97], v[182:185], v[154:157]
	s_waitcnt lgkmcnt(1)
	ds_read_b128 v[182:185], v195 offset:16672
	v_mfma_f32_16x16x32_f16 v[142:145], v[34:37], v[174:177], v[142:145]
	v_mfma_f32_16x16x32_f16 v[146:149], v[38:41], v[174:177], v[146:149]
	v_mfma_f32_16x16x32_f16 v[150:153], v[42:45], v[174:177], v[150:153]
	v_mfma_f32_16x16x32_f16 v[154:157], v[46:49], v[174:177], v[154:157]
	s_waitcnt lgkmcnt(1)
	ds_read_b128 v[174:177], v195 offset:16688
	v_mfma_f32_16x16x32_f16 v[142:145], v[50:53], v[178:181], v[142:145]
	v_mfma_f32_16x16x32_f16 v[146:149], v[54:57], v[178:181], v[146:149]
	v_mfma_f32_16x16x32_f16 v[150:153], v[58:61], v[178:181], v[150:153]
	v_mfma_f32_16x16x32_f16 v[154:157], v[62:65], v[178:181], v[154:157]
	s_waitcnt vmcnt(0)
	s_cmp_ge_u32 s24, 4
	s_cbranch_scc1 .Lskips85
	ds_write_b128 v201, v[186:189] offset:15360
.Lskips85:
	ds_write_b128 v201, v[190:193] offset:1280
	s_waitcnt lgkmcnt(3)
	ds_read_b128 v[178:181], v194 offset:17920
	v_mfma_f32_16x16x32_f16 v[142:145], v[98:101], v[182:185], v[142:145]
	v_mfma_f32_16x16x32_f16 v[146:149], v[102:105], v[182:185], v[146:149]
	v_mfma_f32_16x16x32_f16 v[150:153], v[106:109], v[182:185], v[150:153]
	v_mfma_f32_16x16x32_f16 v[154:157], v[110:113], v[182:185], v[154:157]
	s_waitcnt lgkmcnt(3)
	ds_read_b128 v[182:185], v194 offset:17936
	v_mfma_f32_16x16x32_f16 v[142:145], v[114:117], v[174:177], v[142:145]
	v_mfma_f32_16x16x32_f16 v[146:149], v[118:121], v[174:177], v[146:149]
	v_mfma_f32_16x16x32_f16 v[150:153], v[122:125], v[174:177], v[150:153]
	v_mfma_f32_16x16x32_f16 v[154:157], v[126:129], v[174:177], v[154:157]
	s_waitcnt lgkmcnt(1)
	ds_read_b128 v[174:177], v195 offset:17920
	v_mfma_f32_16x16x32_f16 v[158:161], v[2:5], v[178:181], v[158:161]
	v_mfma_f32_16x16x32_f16 v[162:165], v[6:9], v[178:181], v[162:165]
	v_mfma_f32_16x16x32_f16 v[166:169], v[10:13], v[178:181], v[166:169]
	v_mfma_f32_16x16x32_f16 v[170:173], v[14:17], v[178:181], v[170:173]
	s_waitcnt lgkmcnt(1)
	ds_read_b128 v[178:181], v195 offset:17936
	v_mfma_f32_16x16x32_f16 v[158:161], v[18:21], v[182:185], v[158:161]
	v_mfma_f32_16x16x32_f16 v[162:165], v[22:25], v[182:185], v[162:165]
	v_mfma_f32_16x16x32_f16 v[166:169], v[26:29], v[182:185], v[166:169]
	v_mfma_f32_16x16x32_f16 v[170:173], v[30:33], v[182:185], v[170:173]
	v_exp_f32_e32 v142, v142
	v_exp_f32_e32 v143, v143
	v_exp_f32_e32 v144, v144
	v_exp_f32_e32 v145, v145
	v_exp_f32_e32 v146, v146
	v_exp_f32_e32 v147, v147
	v_exp_f32_e32 v148, v148
	v_exp_f32_e32 v149, v149
	v_exp_f32_e32 v150, v150
	v_exp_f32_e32 v151, v151
	v_exp_f32_e32 v152, v152
	v_exp_f32_e32 v153, v153
	v_exp_f32_e32 v154, v154
	v_exp_f32_e32 v155, v155
	v_exp_f32_e32 v156, v156
	v_exp_f32_e32 v157, v157
	v_add_f32_e32 v150, 1.0, v150
	v_add_f32_e32 v151, 1.0, v151
	v_add_f32_e32 v152, 1.0, v152
	v_add_f32_e32 v153, 1.0, v153
	v_add_f32_e32 v146, 1.0, v146
	v_add_f32_e32 v147, 1.0, v147
	v_add_f32_e32 v148, 1.0, v148
	v_add_f32_e32 v149, 1.0, v149
	v_fma_f32 v142, v142, v150, v150
	v_fma_f32 v143, v143, v151, v151
	v_fma_f32 v144, v144, v152, v152
	v_fma_f32 v145, v145, v153, v153
	v_rcp_f32_e32 v146, v146
	v_rcp_f32_e32 v147, v147
	v_rcp_f32_e32 v148, v148
	v_rcp_f32_e32 v149, v149
	v_fma_f32 v150, v150, v204, s16
	v_fma_f32 v151, v151, v204, s16
	v_fma_f32 v152, v152, v204, s16
	v_fma_f32 v153, v153, v204, s16
	v_rcp_f32_e32 v142, v142
	v_rcp_f32_e32 v143, v143
	v_rcp_f32_e32 v144, v144
	v_rcp_f32_e32 v145, v145
	v_mul_f32_e32 v134, v134, v146
	v_mul_f32_e32 v135, v135, v147
	v_mul_f32_e32 v136, v136, v148
	v_mul_f32_e32 v137, v137, v149
	v_fma_f32 v134, v150, v142, v134
	v_fma_f32 v135, v151, v143, v135
	v_fma_f32 v136, v152, v144, v136
	v_fma_f32 v137, v153, v145, v137
	v_exp_f32_e32 v146, v134
	v_exp_f32_e32 v147, v135
	v_exp_f32_e32 v148, v136
	v_exp_f32_e32 v149, v137
	v_add_f32_e32 v142, 1.0, v146
	v_add_f32_e32 v143, 1.0, v147
	v_add_f32_e32 v144, 1.0, v148
	v_add_f32_e32 v145, 1.0, v149
	v_add_f32_e32 v150, -1.0, v146
	v_add_f32_e32 v151, -1.0, v147
	v_add_f32_e32 v152, -1.0, v148
	v_add_f32_e32 v153, -1.0, v149
	v_fma_f32 v154, v154, v142, v142
	v_fma_f32 v155, v155, v143, v143
	v_fma_f32 v156, v156, v144, v144
	v_fma_f32 v157, v157, v145, v145
	v_rcp_f32_e32 v154, v154
	v_rcp_f32_e32 v155, v155
	v_rcp_f32_e32 v156, v156
	v_rcp_f32_e32 v157, v157
	v_mul_f32_e32 v154, v150, v154
	v_mul_f32_e32 v155, v151, v155
	v_mul_f32_e32 v156, v152, v156
	v_mul_f32_e32 v157, v153, v157
	v_cvt_pk_f16_f32 v154, v154, v155
	v_cvt_pk_f16_f32 v155, v156, v157
	ds_write_b64 v196, v[154:155] offset:1280
	ds_read_b128 v[142:145], v197 offset:0
	ds_read_b128 v[146:149], v197 offset:512
	ds_read_b128 v[150:153], v197 offset:1024
	ds_read_b128 v[154:157], v197 offset:1536
	s_waitcnt lgkmcnt(6)
	ds_read_b128 v[182:185], v194 offset:17952
	v_mfma_f32_16x16x32_f16 v[158:161], v[66:69], v[174:177], v[158:161]
	v_mfma_f32_16x16x32_f16 v[162:165], v[70:73], v[174:177], v[162:165]
	v_mfma_f32_16x16x32_f16 v[166:169], v[74:77], v[174:177], v[166:169]
	v_mfma_f32_16x16x32_f16 v[170:173], v[78:81], v[174:177], v[170:173]
	s_waitcnt lgkmcnt(6)
	ds_read_b128 v[174:177], v194 offset:17968
	v_mfma_f32_16x16x32_f16 v[158:161], v[82:85], v[178:181], v[158:161]
	v_mfma_f32_16x16x32_f16 v[162:165], v[86:89], v[178:181], v[162:165]
	v_mfma_f32_16x16x32_f16 v[166:169], v[90:93], v[178:181], v[166:169]
	v_mfma_f32_16x16x32_f16 v[170:173], v[94:97], v[178:181], v[170:173]
	s_waitcnt lgkmcnt(1)
	ds_read_b128 v[178:181], v195 offset:17952
	v_mfma_f32_16x16x32_f16 v[158:161], v[34:37], v[182:185], v[158:161]
	v_mfma_f32_16x16x32_f16 v[162:165], v[38:41], v[182:185], v[162:165]
	v_mfma_f32_16x16x32_f16 v[166:169], v[42:45], v[182:185], v[166:169]
	v_mfma_f32_16x16x32_f16 v[170:173], v[46:49], v[182:185], v[170:173]
	s_waitcnt lgkmcnt(1)
	ds_read_b128 v[182:185], v195 offset:17968
	v_mfma_f32_16x16x32_f16 v[158:161], v[50:53], v[174:177], v[158:161]
	v_mfma_f32_16x16x32_f16 v[162:165], v[54:57], v[174:177], v[162:165]
	v_mfma_f32_16x16x32_f16 v[166:169], v[58:61], v[174:177], v[166:169]
	v_mfma_f32_16x16x32_f16 v[170:173], v[62:65], v[174:177], v[170:173]
	s_waitcnt lgkmcnt(1)
	ds_read_b128 v[174:177], v194 offset:0
	v_mfma_f32_16x16x32_f16 v[158:161], v[98:101], v[178:181], v[158:161]
	v_mfma_f32_16x16x32_f16 v[162:165], v[102:105], v[178:181], v[162:165]
	v_mfma_f32_16x16x32_f16 v[166:169], v[106:109], v[178:181], v[166:169]
	v_mfma_f32_16x16x32_f16 v[170:173], v[110:113], v[178:181], v[170:173]
	s_waitcnt lgkmcnt(1)
	ds_read_b128 v[178:181], v194 offset:16
	v_mfma_f32_16x16x32_f16 v[158:161], v[114:117], v[182:185], v[158:161]
	v_mfma_f32_16x16x32_f16 v[162:165], v[118:121], v[182:185], v[162:165]
	v_mfma_f32_16x16x32_f16 v[166:169], v[122:125], v[182:185], v[166:169]
	v_mfma_f32_16x16x32_f16 v[170:173], v[126:129], v[182:185], v[170:173]
	s_waitcnt lgkmcnt(1)
	ds_read_b128 v[182:185], v194 offset:32
	v_mfma_f32_16x16x32_f16 v[142:145], v[2:5], v[174:177], v[142:145]
	v_mfma_f32_16x16x32_f16 v[146:149], v[6:9], v[174:177], v[146:149]
	v_mfma_f32_16x16x32_f16 v[150:153], v[10:13], v[174:177], v[150:153]
	v_mfma_f32_16x16x32_f16 v[154:157], v[14:17], v[174:177], v[154:157]
	s_waitcnt lgkmcnt(1)
	ds_read_b128 v[174:177], v194 offset:48
	v_mfma_f32_16x16x32_f16 v[142:145], v[18:21], v[178:181], v[142:145]
	v_mfma_f32_16x16x32_f16 v[146:149], v[22:25], v[178:181], v[146:149]
	v_mfma_f32_16x16x32_f16 v[150:153], v[26:29], v[178:181], v[150:153]
	v_mfma_f32_16x16x32_f16 v[154:157], v[30:33], v[178:181], v[154:157]
	v_exp_f32_e32 v158, v158
	v_exp_f32_e32 v159, v159
	v_exp_f32_e32 v160, v160
	v_exp_f32_e32 v161, v161
	v_exp_f32_e32 v162, v162
	v_exp_f32_e32 v163, v163
	v_exp_f32_e32 v164, v164
	v_exp_f32_e32 v165, v165
	v_exp_f32_e32 v166, v166
	v_exp_f32_e32 v167, v167
	v_exp_f32_e32 v168, v168
	v_exp_f32_e32 v169, v169
	v_exp_f32_e32 v170, v170
	v_exp_f32_e32 v171, v171
	v_exp_f32_e32 v172, v172
	v_exp_f32_e32 v173, v173
	v_add_f32_e32 v166, 1.0, v166
	v_add_f32_e32 v167, 1.0, v167
	v_add_f32_e32 v168, 1.0, v168
	v_add_f32_e32 v169, 1.0, v169
	v_add_f32_e32 v162, 1.0, v162
	v_add_f32_e32 v163, 1.0, v163
	v_add_f32_e32 v164, 1.0, v164
	v_add_f32_e32 v165, 1.0, v165
	v_fma_f32 v158, v158, v166, v166
	v_fma_f32 v159, v159, v167, v167
	v_fma_f32 v160, v160, v168, v168
	v_fma_f32 v161, v161, v169, v169
	v_rcp_f32_e32 v162, v162
	v_rcp_f32_e32 v163, v163
	v_rcp_f32_e32 v164, v164
	v_rcp_f32_e32 v165, v165
	v_fma_f32 v166, v166, v204, s16
	v_fma_f32 v167, v167, v204, s16
	v_fma_f32 v168, v168, v204, s16
	v_fma_f32 v169, v169, v204, s16
	v_rcp_f32_e32 v158, v158
	v_rcp_f32_e32 v159, v159
	v_rcp_f32_e32 v160, v160
	v_rcp_f32_e32 v161, v161
	v_mul_f32_e32 v138, v138, v162
	v_mul_f32_e32 v139, v139, v163
	v_mul_f32_e32 v140, v140, v164
	v_mul_f32_e32 v141, v141, v165
	v_fma_f32 v138, v166, v158, v138
	v_fma_f32 v139, v167, v159, v139
	v_fma_f32 v140, v168, v160, v140
	v_fma_f32 v141, v169, v161, v141
	v_exp_f32_e32 v162, v138
	v_exp_f32_e32 v163, v139
	v_exp_f32_e32 v164, v140
	v_exp_f32_e32 v165, v141
	v_add_f32_e32 v158, 1.0, v162
	v_add_f32_e32 v159, 1.0, v163
	v_add_f32_e32 v160, 1.0, v164
	v_add_f32_e32 v161, 1.0, v165
	v_add_f32_e32 v166, -1.0, v162
	v_add_f32_e32 v167, -1.0, v163
	v_add_f32_e32 v168, -1.0, v164
	v_add_f32_e32 v169, -1.0, v165
	v_fma_f32 v170, v170, v158, v158
	v_fma_f32 v171, v171, v159, v159
	v_fma_f32 v172, v172, v160, v160
	v_fma_f32 v173, v173, v161, v161
	v_rcp_f32_e32 v170, v170
	v_rcp_f32_e32 v171, v171
	v_rcp_f32_e32 v172, v172
	v_rcp_f32_e32 v173, v173
	v_mul_f32_e32 v170, v166, v170
	v_mul_f32_e32 v171, v167, v171
	v_mul_f32_e32 v172, v168, v172
	v_mul_f32_e32 v173, v169, v173
	v_cvt_pk_f16_f32 v170, v170, v171
	v_cvt_pk_f16_f32 v171, v172, v173
	ds_write_b64 v196, v[170:171] offset:2560
	ds_read_b128 v[158:161], v197 offset:0
	ds_read_b128 v[162:165], v197 offset:512
	ds_read_b128 v[166:169], v197 offset:1024
	ds_read_b128 v[170:173], v197 offset:1536
	s_waitcnt lgkmcnt(0)
	s_barrier
	s_add_u32 s17, s17, 2
	s_cmp_lt_u32 s17, 16
	s_cbranch_scc1 .Llstm2_loop
	s_waitcnt lgkmcnt(0)
	s_load_dwordx2 s[4:5], s[0:1], 0x38
	s_load_dwordx2 s[6:7], s[0:1], 0x40
	s_load_dwordx2 s[8:9], s[0:1], 0x48
	s_load_dwordx2 s[10:11], s[0:1], 0x50
	s_load_dwordx2 s[12:13], s[0:1], 0x58
	s_load_dwordx2 s[14:15], s[0:1], 0x60
	v_and_b32_e32 v1, 15, v0
	v_bfe_u32 v205, v0, 4, 2
	v_lshrrev_b32_e32 v206, 6, v0
	s_mul_i32 s22, s2, 48
	v_lshl_add_u32 v200, v206, 2, v205
	v_lshlrev_b32_e32 v200, 4, v200
	v_add_u32_e32 v198, s22, v1
	s_waitcnt lgkmcnt(0)
	v_min_u32_e32 v199, 0x270f, v198
	v_lshl_add_u32 v199, v199, 9, v200
	global_load_dwordx4 v[142:145], v199, s[14:15]
	v_add_u32_e32 v198, 16, v198
	v_min_u32_e32 v199, 0x270f, v198
	v_lshl_add_u32 v199, v199, 9, v200
	global_load_dwordx4 v[146:149], v199, s[14:15]
	v_add_u32_e32 v198, 16, v198
	v_min_u32_e32 v199, 0x270f, v198
	v_lshl_add_u32 v199, v199, 9, v200
	global_load_dwordx4 v[150:153], v199, s[14:15]
	global_load_dwordx4 v[158:161], v200, s[6:7]
	global_load_dwordx4 v[162:165], v200, s[8:9]
	v_and_b32_e32 v1, 63, v0
	v_lshlrev_b32_e32 v1, 4, v1
	v_lshl_add_u32 v1, v206, 10, v1
	global_load_dwordx4 v[2:5], v1, s[4:5]
	v_add_u32_e32 v1, 0x2000, v1
	global_load_dwordx4 v[6:9], v1, s[4:5]
	v_add_u32_e32 v1, 0x2000, v1
	global_load_dwordx4 v[10:13], v1, s[4:5]
	v_add_u32_e32 v1, 0x2000, v1
	global_load_dwordx4 v[14:17], v1, s[4:5]
	v_add_u32_e32 v1, 0x2000, v1
	global_load_dwordx4 v[18:21], v1, s[4:5]
	v_add_u32_e32 v1, 0x2000, v1
	global_load_dwordx4 v[22:25], v1, s[4:5]
	v_add_u32_e32 v1, 0x2000, v1
	global_load_dwordx4 v[26:29], v1, s[4:5]
	v_add_u32_e32 v1, 0x2000, v1
	global_load_dwordx4 v[30:33], v1, s[4:5]
	s_waitcnt vmcnt(0)
	ds_read_b128 v[174:177], v207 offset:0
	ds_read_b128 v[178:181], v207 offset:1280
	ds_read_b128 v[182:185], v207 offset:2560
	s_waitcnt lgkmcnt(2)
	v_mfma_f32_16x16x32_f16 v[142:145], v[2:5], v[174:177], v[142:145]
	ds_read_b128 v[174:177], v207 offset:16
	s_waitcnt lgkmcnt(2)
	v_mfma_f32_16x16x32_f16 v[146:149], v[2:5], v[178:181], v[146:149]
	ds_read_b128 v[178:181], v207 offset:1296
	s_waitcnt lgkmcnt(2)
	v_mfma_f32_16x16x32_f16 v[150:153], v[2:5], v[182:185], v[150:153]
	ds_read_b128 v[182:185], v207 offset:2576
	s_waitcnt lgkmcnt(2)
	v_mfma_f32_16x16x32_f16 v[142:145], v[6:9], v[174:177], v[142:145]
	ds_read_b128 v[174:177], v207 offset:32
	s_waitcnt lgkmcnt(2)
	v_mfma_f32_16x16x32_f16 v[146:149], v[6:9], v[178:181], v[146:149]
	ds_read_b128 v[178:181], v207 offset:1312
	s_waitcnt lgkmcnt(2)
	v_mfma_f32_16x16x32_f16 v[150:153], v[6:9], v[182:185], v[150:153]
	ds_read_b128 v[182:185], v207 offset:2592
	s_waitcnt lgkmcnt(2)
	v_mfma_f32_16x16x32_f16 v[142:145], v[10:13], v[174:177], v[142:145]
	ds_read_b128 v[174:177], v207 offset:48
	s_waitcnt lgkmcnt(2)
	v_mfma_f32_16x16x32_f16 v[146:149], v[10:13], v[178:181], v[146:149]
	ds_read_b128 v[178:181], v207 offset:1328
	s_waitcnt lgkmcnt(2)
	v_mfma_f32_16x16x32_f16 v[150:153], v[10:13], v[182:185], v[150:153]
	ds_read_b128 v[182:185], v207 offset:2608
	s_waitcnt lgkmcnt(2)
	v_mfma_f32_16x16x32_f16 v[142:145], v[14:17], v[174:177], v[142:145]
	ds_read_b128 v[174:177], v195 offset:0
	s_waitcnt lgkmcnt(2)
	v_mfma_f32_16x16x32_f16 v[146:149], v[14:17], v[178:181], v[146:149]
	ds_read_b128 v[178:181], v195 offset:1280
	s_waitcnt lgkmcnt(2)
	v_mfma_f32_16x16x32_f16 v[150:153], v[14:17], v[182:185], v[150:153]
	ds_read_b128 v[182:185], v195 offset:2560
	s_waitcnt lgkmcnt(2)
	v_mfma_f32_16x16x32_f16 v[142:145], v[18:21], v[174:177], v[142:145]
	ds_read_b128 v[174:177], v195 offset:16
	s_waitcnt lgkmcnt(2)
	v_mfma_f32_16x16x32_f16 v[146:149], v[18:21], v[178:181], v[146:149]
	ds_read_b128 v[178:181], v195 offset:1296
	s_waitcnt lgkmcnt(2)
	v_mfma_f32_16x16x32_f16 v[150:153], v[18:21], v[182:185], v[150:153]
	ds_read_b128 v[182:185], v195 offset:2576
	s_waitcnt lgkmcnt(2)
	v_mfma_f32_16x16x32_f16 v[142:145], v[22:25], v[174:177], v[142:145]
	ds_read_b128 v[174:177], v195 offset:32
	s_waitcnt lgkmcnt(2)
	v_mfma_f32_16x16x32_f16 v[146:149], v[22:25], v[178:181], v[146:149]
	ds_read_b128 v[178:181], v195 offset:1312
	s_waitcnt lgkmcnt(2)
	v_mfma_f32_16x16x32_f16 v[150:153], v[22:25], v[182:185], v[150:153]
	ds_read_b128 v[182:185], v195 offset:2592
	s_waitcnt lgkmcnt(2)
	v_mfma_f32_16x16x32_f16 v[142:145], v[26:29], v[174:177], v[142:145]
	ds_read_b128 v[174:177], v195 offset:48
	s_waitcnt lgkmcnt(2)
	v_mfma_f32_16x16x32_f16 v[146:149], v[26:29], v[178:181], v[146:149]
	ds_read_b128 v[178:181], v195 offset:1328
	s_waitcnt lgkmcnt(2)
	v_mfma_f32_16x16x32_f16 v[150:153], v[26:29], v[182:185], v[150:153]
	ds_read_b128 v[182:185], v195 offset:2608
	s_waitcnt lgkmcnt(2)
	v_mfma_f32_16x16x32_f16 v[142:145], v[30:33], v[174:177], v[142:145]
	s_waitcnt lgkmcnt(1)
	v_mfma_f32_16x16x32_f16 v[146:149], v[30:33], v[178:181], v[146:149]
	s_waitcnt lgkmcnt(0)
	v_mfma_f32_16x16x32_f16 v[150:153], v[30:33], v[182:185], v[150:153]
	s_nop 7
	s_nop 1
	v_add_f32_e32 v142, v142, v158
	v_add_f32_e32 v143, v143, v159
	v_add_f32_e32 v144, v144, v160
	v_add_f32_e32 v145, v145, v161
	v_max_f32_e32 v142, 0, v142
	v_max_f32_e32 v143, 0, v143
	v_max_f32_e32 v144, 0, v144
	v_max_f32_e32 v145, 0, v145
	v_mul_f32_e32 v166, v142, v162
	v_fma_f32 v166, v143, v163, v166
	v_fma_f32 v166, v144, v164, v166
	v_fma_f32 v166, v145, v165, v166
	ds_write_b32 v208, v166 offset:0
	v_add_f32_e32 v146, v146, v158
	v_add_f32_e32 v147, v147, v159
	v_add_f32_e32 v148, v148, v160
	v_add_f32_e32 v149, v149, v161
	v_max_f32_e32 v146, 0, v146
	v_max_f32_e32 v147, 0, v147
	v_max_f32_e32 v148, 0, v148
	v_max_f32_e32 v149, 0, v149
	v_mul_f32_e32 v167, v146, v162
	v_fma_f32 v167, v147, v163, v167
	v_fma_f32 v167, v148, v164, v167
	v_fma_f32 v167, v149, v165, v167
	ds_write_b32 v208, v167 offset:2048
	v_add_f32_e32 v150, v150, v158
	v_add_f32_e32 v151, v151, v159
	v_add_f32_e32 v152, v152, v160
	v_add_f32_e32 v153, v153, v161
	v_max_f32_e32 v150, 0, v150
	v_max_f32_e32 v151, 0, v151
	v_max_f32_e32 v152, 0, v152
	v_max_f32_e32 v153, 0, v153
	v_mul_f32_e32 v168, v150, v162
	v_fma_f32 v168, v151, v163, v168
	v_fma_f32 v168, v152, v164, v168
	v_fma_f32 v168, v153, v165, v168
	ds_write_b32 v208, v168 offset:4096
	s_waitcnt lgkmcnt(0)
	s_barrier
	v_add_u32_e32 v205, s22, v0
	s_movk_i32 s23, 0x2710
	v_cmp_gt_u32_e64 s[16:17], s23, v205
	v_cmp_gt_u32_e64 s[18:19], 48, v0
	s_nop 3
	s_and_b64 s[16:17], s[16:17], s[18:19]
	s_and_saveexec_b64 s[18:19], s[16:17]
	s_cbranch_execz .Ll2_end
	v_lshlrev_b32_e32 v1, 7, v0
	v_add_u32_e32 v1, 0x13400, v1
	ds_read_b128 v[2:5], v1 offset:0
	ds_read_b128 v[6:9], v1 offset:16
	ds_read_b128 v[10:13], v1 offset:32
	ds_read_b128 v[14:17], v1 offset:48
	ds_read_b128 v[18:21], v1 offset:64
	ds_read_b128 v[22:25], v1 offset:80
	ds_read_b128 v[26:29], v1 offset:96
	ds_read_b128 v[30:33], v1 offset:112
	s_load_dword s20, s[10:11], 0x0
	s_waitcnt lgkmcnt(0)
	v_mov_b32_e32 v206, s20
	v_add_f32_e32 v206, v206, v2
	v_add_f32_e32 v206, v206, v3
	v_add_f32_e32 v206, v206, v4
	v_add_f32_e32 v206, v206, v5
	v_add_f32_e32 v206, v206, v6
	v_add_f32_e32 v206, v206, v7
	v_add_f32_e32 v206, v206, v8
	v_add_f32_e32 v206, v206, v9
	v_add_f32_e32 v206, v206, v10
	v_add_f32_e32 v206, v206, v11
	v_add_f32_e32 v206, v206, v12
	v_add_f32_e32 v206, v206, v13
	v_add_f32_e32 v206, v206, v14
	v_add_f32_e32 v206, v206, v15
	v_add_f32_e32 v206, v206, v16
	v_add_f32_e32 v206, v206, v17
	v_add_f32_e32 v206, v206, v18
	v_add_f32_e32 v206, v206, v19
	v_add_f32_e32 v206, v206, v20
	v_add_f32_e32 v206, v206, v21
	v_add_f32_e32 v206, v206, v22
	v_add_f32_e32 v206, v206, v23
	v_add_f32_e32 v206, v206, v24
	v_add_f32_e32 v206, v206, v25
	v_add_f32_e32 v206, v206, v26
	v_add_f32_e32 v206, v206, v27
	v_add_f32_e32 v206, v206, v28
	v_add_f32_e32 v206, v206, v29
	v_add_f32_e32 v206, v206, v30
	v_add_f32_e32 v206, v206, v31
	v_add_f32_e32 v206, v206, v32
	v_add_f32_e32 v206, v206, v33
	v_max_f32_e32 v206, 0, v206
	v_lshlrev_b32_e32 v205, 2, v205
	global_store_dword v205, v206, s[12:13]
